# dense attention K tile LDS-DMA: each request gathers 16 rows x 64 B instead of 64 rows x 16 B; matching K fragment read addresses
# baseline (speedup 1.0000x reference)
.LBB0_241:
	s_or_b64 exec, exec, s[14:15]
	s_waitcnt lgkmcnt(0)
	v_add_u32_e32 v0, s11, v213
	ds_read_b128 v[36:39], v0 offset:128
	ds_read_b128 v[40:43], v0 offset:160
	s_add_u32 s10, s8, s90
	s_addc_u32 s11, s9, s91
	s_lshl_b32 s14, s42, 12
	s_waitcnt lgkmcnt(1)
	v_rcp_f32_e32 v2, v36
	v_rcp_f32_e32 v44, v37
	v_rcp_f32_e32 v45, v38
	v_rcp_f32_e32 v46, v39
	s_waitcnt lgkmcnt(0)
	v_rcp_f32_e32 v47, v40
	ds_read_b128 v[36:39], v0 offset:192
	v_rcp_f32_e32 v48, v41
	v_rcp_f32_e32 v49, v42
	v_rcp_f32_e32 v50, v43
	ds_read_b128 v[40:43], v0 offset:224
	s_waitcnt lgkmcnt(1)
	v_rcp_f32_e32 v0, v36
	v_rcp_f32_e32 v36, v37
	v_rcp_f32_e32 v37, v38
	v_rcp_f32_e32 v38, v39
	s_waitcnt lgkmcnt(0)
	v_rcp_f32_e32 v39, v40
	v_rcp_f32_e32 v40, v41
	v_rcp_f32_e32 v41, v42
	v_rcp_f32_e32 v42, v43
	s_add_i32 s14, s14, 0
	v_lshlrev_b32_e32 v43, 1, v207
	v_mul_f32_e32 v4, v4, v2
	v_mul_f32_e32 v2, v20, v2
	v_add3_u32 v43, s14, v202, v43
	v_cvt_pk_bf16_f32 v2, v2, s0
	ds_write_b16 v43, v2 offset:64
	v_mul_f32_e32 v2, v5, v44
	v_cvt_pk_bf16_f32 v2, v2, s0
	ds_write_b16 v43, v2 offset:128
	v_mul_f32_e32 v2, v21, v44
	v_cvt_pk_bf16_f32 v2, v2, s0
	ds_write_b16 v43, v2 offset:192
	v_mul_f32_e32 v2, v6, v45
	v_cvt_pk_bf16_f32 v2, v2, s0
	ds_write_b16 v43, v2 offset:256
	v_mul_f32_e32 v2, v22, v45
	v_cvt_pk_bf16_f32 v2, v2, s0
	ds_write_b16 v43, v2 offset:320
	v_mul_f32_e32 v2, v7, v46
	v_cvt_pk_bf16_f32 v2, v2, s0
	ds_write_b16 v43, v2 offset:384
	v_mul_f32_e32 v2, v23, v46
	v_cvt_pk_bf16_f32 v2, v2, s0
	ds_write_b16 v43, v2 offset:448
	v_mul_f32_e32 v2, v8, v47
	v_cvt_pk_bf16_f32 v2, v2, s0
	ds_write_b16 v43, v2 offset:1024
	v_mul_f32_e32 v2, v24, v47
	v_cvt_pk_bf16_f32 v2, v2, s0
	ds_write_b16 v43, v2 offset:1088
	v_mul_f32_e32 v2, v9, v48
	v_cvt_pk_bf16_f32 v2, v2, s0
	ds_write_b16 v43, v2 offset:1152
	v_mul_f32_e32 v2, v25, v48
	v_cvt_pk_bf16_f32 v2, v2, s0
	ds_write_b16 v43, v2 offset:1216
	v_mul_f32_e32 v2, v10, v49
	v_cvt_pk_bf16_f32 v2, v2, s0
	ds_write_b16 v43, v2 offset:1280
	v_mul_f32_e32 v2, v26, v49
	v_cvt_pk_bf16_f32 v2, v2, s0
	ds_write_b16 v43, v2 offset:1344
	v_mul_f32_e32 v2, v11, v50
	v_cvt_pk_bf16_f32 v2, v2, s0
	ds_write_b16 v43, v2 offset:1408
	v_mul_f32_e32 v2, v27, v50
	v_cvt_pk_bf16_f32 v2, v2, s0
	ds_write_b16 v43, v2 offset:1472
	v_mul_f32_e32 v2, v12, v0
	v_mul_f32_e32 v0, v28, v0
	v_cvt_pk_bf16_f32 v0, v0, s0
	ds_write_b16 v43, v0 offset:2112
	v_mul_f32_e32 v0, v13, v36
	v_cvt_pk_bf16_f32 v0, v0, s0
	ds_write_b16 v43, v0 offset:2176
	v_mul_f32_e32 v0, v29, v36
	v_cvt_pk_bf16_f32 v0, v0, s0
	ds_write_b16 v43, v0 offset:2240
	v_mul_f32_e32 v0, v14, v37
	v_cvt_pk_bf16_f32 v0, v0, s0
	ds_write_b16 v43, v0 offset:2304
	v_mul_f32_e32 v0, v30, v37
	v_cvt_pk_bf16_f32 v0, v0, s0
	ds_write_b16 v43, v0 offset:2368
	v_mul_f32_e32 v0, v15, v38
	v_cvt_pk_bf16_f32 v0, v0, s0
	ds_write_b16 v43, v0 offset:2432
	v_mul_f32_e32 v0, v31, v38
	v_cvt_pk_bf16_f32 v0, v0, s0
	ds_write_b16 v43, v0 offset:2496
	v_mul_f32_e32 v0, v16, v39
	v_cvt_pk_bf16_f32 v0, v0, s0
	ds_write_b16 v43, v0 offset:3072
	v_mul_f32_e32 v0, v32, v39
	v_cvt_pk_bf16_f32 v0, v0, s0
	ds_write_b16 v43, v0 offset:3136
	v_mul_f32_e32 v0, v17, v40
	v_cvt_pk_bf16_f32 v0, v0, s0
	ds_write_b16 v43, v0 offset:3200
	v_mul_f32_e32 v0, v33, v40
	v_cvt_pk_bf16_f32 v0, v0, s0
	ds_write_b16 v43, v0 offset:3264
	v_mul_f32_e32 v0, v18, v41
	v_cvt_pk_bf16_f32 v0, v0, s0
	ds_write_b16 v43, v0 offset:3328
	v_mul_f32_e32 v0, v34, v41
	v_cvt_pk_bf16_f32 v0, v0, s0
	ds_write_b16 v43, v0 offset:3392
	v_mul_f32_e32 v0, v19, v42
	v_cvt_pk_bf16_f32 v0, v0, s0
	v_cvt_pk_bf16_f32 v2, v2, s0
	ds_write_b16 v43, v0 offset:3456
	v_mul_f32_e32 v0, v35, v42
	v_cvt_pk_bf16_f32 v4, v4, s0
	ds_write_b16 v43, v2 offset:2048
	v_cvt_pk_bf16_f32 v0, v0, s0
	s_add_u32 s10, s10, vcc_lo
	v_lshlrev_b32_e32 v2, 1, v200
	ds_write_b16 v43, v4
	ds_write_b16 v43, v0 offset:3520
	s_addc_u32 s11, s11, vcc_hi
	v_add_u32_e32 v0, s14, v2
	s_waitcnt lgkmcnt(0)
	v_lshl_add_u64 v[8:9], s[10:11], 0, v[2:3]
	v_add_u32_e32 v2, v0, v203
	ds_read_b128 v[4:7], v2
	v_lshlrev_b32_e32 v2, 1, v196
	v_lshl_add_u64 v[12:13], v[8:9], 0, v[2:3]
	v_add_u32_e32 v2, v0, v204
	ds_read_b128 v[8:11], v2
	s_waitcnt lgkmcnt(1)
	global_store_dwordx4 v[12:13], v[4:7], off
	v_add_u32_e32 v2, v0, v205
	v_add_u32_e32 v0, v0, v206
	v_add_co_u32_e32 v4, vcc, 0x6000, v12
	s_nop 1
	v_addc_co_u32_e32 v5, vcc, 0, v13, vcc
	s_waitcnt lgkmcnt(0)
	global_store_dwordx4 v[4:5], v[8:11], off
	ds_read_b128 v[4:7], v2
	ds_read_b128 v[8:11], v0
	v_add_co_u32_e32 v14, vcc, 0xc000, v12
	s_nop 1
	v_addc_co_u32_e32 v15, vcc, 0, v13, vcc
	s_waitcnt lgkmcnt(1)
	global_store_dwordx4 v[14:15], v[4:7], off
	s_nop 1
	v_add_co_u32_e32 v4, vcc, 0x12000, v12
	s_nop 1
	v_addc_co_u32_e32 v5, vcc, 0, v13, vcc
	s_waitcnt lgkmcnt(0)
	global_store_dwordx4 v[4:5], v[8:11], off
	s_waitcnt lgkmcnt(0)
	s_barrier
	v_mbcnt_lo_u32_b32 v0, -1, 0
	v_mbcnt_hi_u32_b32 v0, -1, v0
	v_lshrrev_b32_e32 v2, 5, v0
	v_and_b32_e32 v0, 31, v0
	v_lshlrev_b32_e32 v0, 4, v0
	v_lshl_add_u32 v210, v2, 10, v0

.LBB0_334:
	s_and_b64 vcc, exec, s[60:61]
	s_cbranch_vccz .LBB0_242
	v_readlane_b32 s10, v254, 20
	s_add_u32 s10, s10, s56
	v_readlane_b32 s11, v254, 19
	s_addc_u32 s11, s11, s57
	s_add_u32 s14, s10, s58
	s_addc_u32 s15, s11, s59
	s_lshl_b64 s[90:91], s[54:55], 1
	s_add_u32 s10, s73, s90
	v_readfirstlane_b32 s11, v235
	s_addc_u32 s44, s75, s91
	s_lshr_b32 s42, s11, 6
	s_lshl_b32 s53, s42, 5
	s_mul_i32 s54, s42, 0xc000
	s_mul_hi_u32 s55, s53, 0x600
	s_lshl_b64 vcc, s[54:55], 1
	s_add_u32 s62, s10, vcc_lo
	s_addc_u32 s63, s44, vcc_hi
	s_lshl_b32 s10, s42, 4
	v_mbcnt_lo_u32_b32 v36, -1, 0
	v_mbcnt_hi_u32_b32 v36, -1, v36
	v_and_b32_e32 v37, 15, v36
	v_mul_u32_u24_e32 v37, 0x300, v37
	v_lshrrev_b32_e32 v38, 4, v36
	v_lshl_add_u32 v37, v38, 4, v37
	s_and_b32 s53, s42, 3
	s_mul_i32 s53, s53, 0x3000
	s_lshr_b32 s54, s42, 2
	s_lshl_b32 s54, s54, 6
	s_add_i32 s53, s53, s54
	v_add_u32_e32 v165, s53, v37
	v_bfe_u32 v37, v36, 4, 1
	v_lshlrev_b32_e32 v37, 10, v37
	v_lshrrev_b32_e32 v38, 5, v36
	v_lshl_add_u32 v37, v38, 8, v37
	v_and_b32_e32 v38, 15, v36
	v_lshl_add_u32 v210, v38, 4, v37
	v_and_or_b32 v0, s10, 48, v201
	s_lshr_b32 s10, s11, 3
	s_and_b32 s10, s10, 0x1fffffe0
	s_lshl_b32 s44, s42, 10
	v_mov_b32_e32 v2, s10
	s_movk_i32 s10, 0x180
	s_cmp_lg_u32 0, -1
	v_mad_u32_u24 v0, v0, s10, v2
	s_cselect_b32 s10, 0, 0
	s_add_i32 s70, s44, s10
	v_or_b32_e32 v0, v0, v209
	s_add_i32 s10, s70, 0xc000
	s_mov_b32 m0, s70
	s_nop 0
	global_load_lds_dwordx4 v165, s[88:89]
	v_lshlrev_b32_e32 v164, 1, v0
	s_mov_b32 m0, s10
	s_nop 0
	global_load_lds_dwordx4 v164, s[14:15]
	s_add_u32 s54, s88, 0xc000
	s_addc_u32 s55, s89, 0
	s_add_i32 s71, s70, 0x2000
	s_mov_b32 m0, s71
	s_nop 0
	global_load_lds_dwordx4 v165, s[54:55]
	global_load_dwordx4 v[140:143], v217, s[62:63]
	global_load_dwordx4 v[128:131], v217, s[62:63] offset:32
	global_load_dwordx4 v[136:139], v217, s[62:63] offset:64
	global_load_dwordx4 v[132:135], v217, s[62:63] offset:96
	s_add_u32 s64, s88, 0x18000
	s_addc_u32 s65, s89, 0
	s_add_i32 s76, s70, 0x4000
	s_add_u32 s62, s88, 0x24000
	s_mov_b32 m0, s76
	s_nop 0
	global_load_lds_dwordx4 v165, s[64:65]
	s_addc_u32 s63, s89, 0
	s_add_i32 s77, s70, 0x6000
	s_mov_b32 m0, s77
	s_nop 0
	global_load_lds_dwordx4 v165, s[62:63]
	s_add_u32 s62, s14, 0xc000
	s_addc_u32 s63, s15, 0
	s_add_i32 s78, s70, 0xe000
	s_mov_b32 m0, s78
	s_nop 0
	global_load_lds_dwordx4 v164, s[62:63]
	s_add_u32 s62, s88, 0x30000
	s_addc_u32 s63, s89, 0
	s_add_i32 s79, s70, 0x8000
	s_mov_b32 m0, s79
	s_nop 0
	global_load_lds_dwordx4 v165, s[62:63]
	s_add_u32 s62, s88, 0x3c000
	s_addc_u32 s63, s89, 0
	s_add_i32 s85, s70, 0xa000
	s_mov_b32 m0, s85
	s_nop 0
	global_load_lds_dwordx4 v165, s[62:63]
	s_add_u32 s62, s14, 0x18000
	s_addc_u32 s63, s15, 0
	s_add_i32 s92, s70, 0x10000
	s_mov_b32 m0, s92
	s_nop 0
	global_load_lds_dwordx4 v164, s[62:63]
	s_add_u32 s62, s14, 0x24000
	s_addc_u32 s63, s15, 0
	s_add_i32 s93, s70, 0x12000
	s_mov_b32 m0, s93
	s_nop 0
	global_load_lds_dwordx4 v164, s[62:63]
	s_waitcnt vmcnt(7) lgkmcnt(0)
	s_barrier
	s_waitcnt vmcnt(22)
	ds_read_b128 v[36:39], v210
	s_waitcnt vmcnt(21)
	ds_read_b128 v[40:43], v210 offset:2048
	s_mov_b32 s53, s52
	s_mov_b32 s54, s52
	s_mov_b32 s55, s52
	s_mov_b32 s56, s52
	s_mov_b32 s57, s52
	s_mov_b32 s58, s52
	s_mov_b32 s59, s52
	s_mov_b32 s60, s52
	s_mov_b32 s61, s52
	s_mov_b32 s62, s52
	s_mov_b32 s63, s52
	s_mov_b32 s64, s52
	s_mov_b32 s65, s52
	s_mov_b32 s66, s52
	s_mov_b32 s67, s52
	s_waitcnt vmcnt(13)
	v_mov_b64_e32 v[4:5], s[52:53]
	v_mov_b64_e32 v[6:7], s[54:55]
	v_mov_b64_e32 v[8:9], s[56:57]
	v_mov_b64_e32 v[10:11], s[58:59]
	v_mov_b64_e32 v[12:13], s[60:61]
	v_mov_b64_e32 v[14:15], s[62:63]
	v_mov_b64_e32 v[16:17], s[64:65]
	v_mov_b64_e32 v[18:19], s[66:67]
	v_mov_b32_e32 v148, 0
	v_mov_b32_e32 v2, 0
	v_mov_b32_e32 v72, 0
	s_mov_b32 s53, -5
	s_waitcnt lgkmcnt(1)
	v_mfma_f32_32x32x16_bf16 v[20:35], v[36:39], v[140:143], v[4:19]
	s_mov_b64 s[54:55], 0
	v_mov_b32_e32 v73, 0
	v_mov_b32_e32 v149, v148
	v_mov_b32_e32 v150, v148
	v_mov_b32_e32 v151, v148
	s_waitcnt lgkmcnt(0)
	v_mfma_f32_32x32x16_bf16 v[4:19], v[40:43], v[140:143], v[4:19]
	ds_read_b128 v[36:39], v210 offset:512
	ds_read_b128 v[40:43], v210 offset:2560
	s_waitcnt lgkmcnt(1)
	v_mfma_f32_32x32x16_bf16 v[20:35], v[36:39], v[128:131], v[20:35]
	s_waitcnt lgkmcnt(0)
	v_mfma_f32_32x32x16_bf16 v[4:19], v[40:43], v[128:131], v[4:19]
	ds_read_b128 v[36:39], v210 offset:4096
	ds_read_b128 v[40:43], v210 offset:6144
	s_waitcnt lgkmcnt(1)
	v_mfma_f32_32x32x16_bf16 v[20:35], v[36:39], v[136:139], v[20:35]
	s_waitcnt lgkmcnt(0)
	v_mfma_f32_32x32x16_bf16 v[4:19], v[40:43], v[136:139], v[4:19]
	ds_read_b128 v[36:39], v210 offset:4608
	ds_read_b128 v[40:43], v210 offset:6656
	s_waitcnt lgkmcnt(1)
	v_mfma_f32_32x32x16_bf16 v[20:35], v[36:39], v[132:135], v[20:35]
	s_waitcnt lgkmcnt(0)
	v_mfma_f32_32x32x16_bf16 v[4:19], v[40:43], v[132:135], v[4:19]
	s_nop 15
	s_nop 7
	s_waitcnt vmcnt(4) lgkmcnt(0)
	s_barrier
	ds_read_b128 v[68:71], v210 offset:8192
	ds_read_b128 v[160:163], v210 offset:10240
	ds_read_b128 v[156:159], v210 offset:8704
	ds_read_b128 v[112:115], v210 offset:10752
	ds_read_b128 v[152:155], v210 offset:12288
	ds_read_b128 v[104:107], v210 offset:14336
	ds_read_b128 v[108:111], v210 offset:12800
	ds_read_b128 v[100:103], v210 offset:14848
	s_nop 1
	v_exp_f32_e32 v52, v20
	v_exp_f32_e32 v53, v21
	v_exp_f32_e32 v54, v22
	v_exp_f32_e32 v55, v23
	v_exp_f32_e32 v56, v24
	v_exp_f32_e32 v57, v25
	v_exp_f32_e32 v58, v26
	v_exp_f32_e32 v59, v27
	v_exp_f32_e32 v60, v28
	v_exp_f32_e32 v61, v29
	v_exp_f32_e32 v62, v30
	v_exp_f32_e32 v63, v31
	v_exp_f32_e32 v64, v32
	v_exp_f32_e32 v65, v33
	v_exp_f32_e32 v66, v34
	v_exp_f32_e32 v67, v35
	v_exp_f32_e32 v36, v4
	v_exp_f32_e32 v37, v5
	v_exp_f32_e32 v38, v6
	v_exp_f32_e32 v39, v7
	v_exp_f32_e32 v40, v8
	v_exp_f32_e32 v41, v9
	v_exp_f32_e32 v42, v10
	v_exp_f32_e32 v43, v11
	v_mov_b32_e32 v44, v12
	v_mov_b32_e32 v45, v13
	v_mov_b32_e32 v46, v14
	v_mov_b32_e32 v47, v15
	v_mov_b32_e32 v48, v16
	v_mov_b32_e32 v49, v17
	v_mov_b32_e32 v50, v18
	v_mov_b32_e32 v51, v19
	s_waitcnt vmcnt(4) lgkmcnt(0)
	s_barrier
	v_mov_b32_e32 v4, 0
	v_mov_b32_e32 v5, v2
	v_mov_b32_e32 v6, v2
	v_mov_b32_e32 v7, v2
	v_mov_b32_e32 v8, v2
	v_mov_b32_e32 v9, v2
	v_mov_b32_e32 v10, v2
	v_mov_b32_e32 v11, v2
	v_mov_b32_e32 v12, v2
	v_mov_b32_e32 v13, v2
	v_mov_b32_e32 v14, v2
	v_mov_b32_e32 v15, v2
	v_mov_b32_e32 v16, v2
	v_mov_b32_e32 v17, v2
	v_mov_b32_e32 v18, v2
	v_mov_b32_e32 v19, v2
	v_mov_b32_e32 v20, 0
	v_mov_b32_e32 v21, v2
	v_mov_b32_e32 v22, v2
	v_mov_b32_e32 v23, v2
	v_mov_b32_e32 v24, v2
	v_mov_b32_e32 v25, v2
	v_mov_b32_e32 v26, v2
	v_mov_b32_e32 v27, v2
	v_mov_b32_e32 v28, v2
	v_mov_b32_e32 v29, v2
	v_mov_b32_e32 v30, v2
	v_mov_b32_e32 v31, v2
	v_mov_b32_e32 v32, v2
	v_mov_b32_e32 v33, v2
	v_mov_b32_e32 v34, v2
	v_mov_b32_e32 v35, v2
.LBB0_336:
	ds_read_b64_tr_b16 v[144:145], v211 offset:49152
	ds_read_b64_tr_b16 v[146:147], v211 offset:49664
	s_waitcnt lgkmcnt(9)
	v_mfma_f32_32x32x16_bf16 v[84:99], v[68:71], v[140:143], -4.0
	v_pk_add_f16 v0, v72, v150
	v_pk_add_f16 v68, v73, v151
	v_cvt_pk_f16_f32 v124, v52, v53
	v_pk_add_f16 v0, v0, v68
	v_cvt_pk_f16_f32 v125, v54, v55
	v_dot2c_f32_f16_e32 v2, 0x3c003c00, v0
	ds_read_b64_tr_b16 v[52:53], v211 offset:53248
	ds_read_b64_tr_b16 v[54:55], v211 offset:53760
	s_waitcnt lgkmcnt(10)
	v_mfma_f32_32x32x16_bf16 v[68:83], v[160:163], v[140:143], -4.0
	v_exp_f32_e32 v44, v44
	v_cvt_pk_f16_f32 v126, v56, v57
	v_cvt_pk_f16_f32 v127, v58, v59
	ds_read_b64_tr_b16 v[56:57], v211 offset:50176
	ds_read_b64_tr_b16 v[58:59], v211 offset:50688
	s_waitcnt lgkmcnt(11)
	v_mfma_f32_32x32x16_bf16 v[84:99], v[156:159], v[128:131], v[84:99]
	v_exp_f32_e32 v45, v45
	v_pk_add_f16 v0, v124, v126
	v_pk_add_f16 v116, v125, v127
	v_cvt_pk_f16_f32 v120, v60, v61
	v_cvt_pk_f16_f32 v121, v62, v63
	ds_read_b64_tr_b16 v[60:61], v211 offset:54272
	ds_read_b64_tr_b16 v[62:63], v211 offset:54784
	s_waitcnt lgkmcnt(12)
	v_mfma_f32_32x32x16_bf16 v[68:83], v[112:115], v[128:131], v[68:83]
	v_exp_f32_e32 v46, v46
	v_exp_f32_e32 v47, v47
	v_pk_add_f16 v0, v0, v120
	v_pk_add_f16 v116, v116, v121
	v_cvt_pk_f16_f32 v122, v64, v65
	v_cvt_pk_f16_f32 v123, v66, v67
	ds_read_b64_tr_b16 v[64:65], v211 offset:51200
	ds_read_b64_tr_b16 v[66:67], v211 offset:51712
	s_waitcnt lgkmcnt(13)
	v_mfma_f32_32x32x16_bf16 v[84:99], v[152:155], v[136:139], v[84:99]
	v_exp_f32_e32 v48, v48
	v_exp_f32_e32 v49, v49
	v_pk_add_f16 v0, v0, v122
	v_pk_add_f16 v112, v116, v123
	v_cvt_pk_f16_f32 v116, v36, v37
	v_cvt_pk_f16_f32 v117, v38, v39
	ds_read_b64_tr_b16 v[36:37], v211 offset:55296
	ds_read_b64_tr_b16 v[38:39], v211 offset:55808
	s_waitcnt lgkmcnt(14)
	v_mfma_f32_32x32x16_bf16 v[68:83], v[104:107], v[136:139], v[68:83]
	v_exp_f32_e32 v50, v50
	v_pk_add_f16 v0, v0, v116
	v_pk_add_f16 v112, v112, v117
	v_cvt_pk_f16_f32 v118, v40, v41
	v_cvt_pk_f16_f32 v119, v42, v43
	ds_read_b64_tr_b16 v[40:41], v211 offset:52224
	ds_read_b64_tr_b16 v[42:43], v211 offset:52736
	v_cvt_pk_f16_f32 v148, v44, v45
	v_pk_add_f16 v0, v0, v118
	v_pk_add_f16 v104, v112, v119
	v_cvt_pk_f16_f32 v149, v46, v47
	s_waitcnt lgkmcnt(14)
	v_mfma_f32_32x32x16_bf16 v[84:99], v[108:111], v[132:135], v[84:99]
	v_exp_f32_e32 v51, v51
	ds_read_b64_tr_b16 v[44:45], v211 offset:56320
	ds_read_b64_tr_b16 v[46:47], v211 offset:56832
	v_mfma_f32_32x32x16_bf16 v[68:83], v[100:103], v[132:135], v[68:83]
	v_pk_add_f16 v0, v0, v148
	v_pk_add_f16 v166, v104, v149
	v_cvt_pk_f16_f32 v150, v48, v49
	v_cvt_pk_f16_f32 v151, v50, v51
	s_add_u32 s56, s88, s54
	s_addc_u32 s57, s89, s55
	s_add_u32 s58, s56, 0x48000
	s_addc_u32 s59, s57, 0
	s_mov_b32 m0, s70
	s_nop 0
	global_load_lds_dwordx4 v165, s[58:59]
	s_add_u32 s58, s14, s54
	s_addc_u32 s59, s15, s55
	s_add_u32 s62, s58, 0x30000
	s_addc_u32 s63, s59, 0
	s_cmp_lg_u32 0, -1
	s_cselect_b32 s60, 0, 0
	s_add_i32 s60, s60, s44
	s_add_i32 s61, s60, 0x14000
	s_mov_b32 m0, s61
	s_nop 0
	global_load_lds_dwordx4 v164, s[62:63]
	s_waitcnt lgkmcnt(14)
	v_mfma_f32_32x32x16_f16 v[4:19], v[124:127], v[144:147], v[4:19]
	v_exp_f32_e32 v84, v84
	v_exp_f32_e32 v85, v85
	v_exp_f32_e32 v86, v86
	s_waitcnt lgkmcnt(12)
	v_mfma_f32_32x32x16_f16 v[20:35], v[124:127], v[52:55], v[20:35]
	v_exp_f32_e32 v87, v87
	v_exp_f32_e32 v88, v88
	v_exp_f32_e32 v89, v89
	ds_read_b128 v[48:51], v210 offset:16384
	ds_read_b128 v[52:55], v210 offset:18432
	s_waitcnt lgkmcnt(12)
	v_mfma_f32_32x32x16_f16 v[4:19], v[120:123], v[56:59], v[4:19]
	v_exp_f32_e32 v90, v90
	v_exp_f32_e32 v91, v91
	v_exp_f32_e32 v92, v92
	ds_read_b128 v[56:59], v210 offset:16896
	ds_read_b128 v[144:147], v210 offset:18944
	s_waitcnt lgkmcnt(12)
	v_mfma_f32_32x32x16_f16 v[20:35], v[120:123], v[60:63], v[20:35]
	v_exp_f32_e32 v93, v93
	v_exp_f32_e32 v94, v94
	v_exp_f32_e32 v95, v95
	ds_read_b128 v[60:63], v210 offset:20480
	ds_read_b128 v[152:155], v210 offset:22528
	s_waitcnt lgkmcnt(12)
	v_mfma_f32_32x32x16_f16 v[4:19], v[116:119], v[64:67], v[4:19]
	v_exp_f32_e32 v96, v96
	v_exp_f32_e32 v97, v97
	v_exp_f32_e32 v98, v98
	ds_read_b128 v[64:67], v210 offset:20992
	ds_read_b128 v[156:159], v210 offset:23040
	s_waitcnt lgkmcnt(12)
	v_mfma_f32_32x32x16_f16 v[20:35], v[116:119], v[36:39], v[20:35]
	v_exp_f32_e32 v99, v99
	v_exp_f32_e32 v68, v68
	v_exp_f32_e32 v69, v69
	s_waitcnt lgkmcnt(10)
	v_mfma_f32_32x32x16_f16 v[4:19], v[148:151], v[40:43], v[4:19]
	v_exp_f32_e32 v70, v70
	v_exp_f32_e32 v71, v71
	v_exp_f32_e32 v72, v72
	s_waitcnt lgkmcnt(8)
	v_mfma_f32_32x32x16_f16 v[20:35], v[148:151], v[44:47], v[20:35]
	v_exp_f32_e32 v73, v73
	v_exp_f32_e32 v74, v74
	v_exp_f32_e32 v75, v75
	ds_read_b64_tr_b16 v[160:161], v211 offset:57344
	ds_read_b64_tr_b16 v[162:163], v211 offset:57856
	s_waitcnt lgkmcnt(9)
	v_mfma_f32_32x32x16_bf16 v[100:115], v[48:51], v[140:143], -4.0
	v_exp_f32_e32 v76, v76
	v_cvt_pk_f16_f32 v124, v84, v85
	v_pk_add_f16 v0, v0, v150
	v_pk_add_f16 v116, v166, v151
	v_cvt_pk_f16_f32 v125, v86, v87
	ds_read_b64_tr_b16 v[84:85], v211 offset:61440
	ds_read_b64_tr_b16 v[86:87], v211 offset:61952
	s_waitcnt lgkmcnt(10)
	v_mfma_f32_32x32x16_bf16 v[36:51], v[52:55], v[140:143], -4.0
	v_exp_f32_e32 v77, v77
	v_pk_add_f16 v0, v0, v124
	v_pk_add_f16 v116, v116, v125
	v_cvt_pk_f16_f32 v126, v88, v89
	v_cvt_pk_f16_f32 v127, v90, v91
	ds_read_b64_tr_b16 v[52:53], v211 offset:58368
	ds_read_b64_tr_b16 v[54:55], v211 offset:58880
	s_waitcnt lgkmcnt(11)
	v_mfma_f32_32x32x16_bf16 v[100:115], v[56:59], v[128:131], v[100:115]
	v_exp_f32_e32 v78, v78
	v_cvt_pk_f16_f32 v120, v92, v93
	v_pk_add_f16 v0, v0, v126
	v_pk_add_f16 v88, v116, v127
	v_cvt_pk_f16_f32 v121, v94, v95
	ds_read_b64_tr_b16 v[56:57], v211 offset:62464
	ds_read_b64_tr_b16 v[58:59], v211 offset:62976
	s_waitcnt lgkmcnt(12)
	v_mfma_f32_32x32x16_bf16 v[36:51], v[144:147], v[128:131], v[36:51]
	v_exp_f32_e32 v79, v79
	v_exp_f32_e32 v80, v80
	v_pk_add_f16 v0, v0, v120
	v_pk_add_f16 v92, v88, v121
	v_cvt_pk_f16_f32 v122, v96, v97
	v_cvt_pk_f16_f32 v123, v98, v99
	ds_read_b64_tr_b16 v[88:89], v211 offset:59392
	ds_read_b64_tr_b16 v[90:91], v211 offset:59904
	s_waitcnt lgkmcnt(13)
	v_mfma_f32_32x32x16_bf16 v[100:115], v[60:63], v[136:139], v[100:115]
	v_exp_f32_e32 v81, v81
	v_cvt_pk_f16_f32 v116, v68, v69
	v_pk_add_f16 v0, v0, v122
	v_pk_add_f16 v92, v92, v123
	v_cvt_pk_f16_f32 v117, v70, v71
	ds_read_b64_tr_b16 v[60:61], v211 offset:63488
	ds_read_b64_tr_b16 v[62:63], v211 offset:64000
	s_waitcnt lgkmcnt(14)
	v_mfma_f32_32x32x16_bf16 v[36:51], v[152:155], v[136:139], v[36:51]
	v_exp_f32_e32 v82, v82
	v_pk_add_f16 v0, v0, v116
	v_pk_add_f16 v92, v92, v117
	v_cvt_pk_f16_f32 v118, v72, v73
	v_cvt_pk_f16_f32 v119, v74, v75
	ds_read_b64_tr_b16 v[68:69], v211 offset:60416
	ds_read_b64_tr_b16 v[70:71], v211 offset:60928
	s_waitcnt lgkmcnt(14)
	v_mfma_f32_32x32x16_bf16 v[100:115], v[64:67], v[132:135], v[100:115]
	v_exp_f32_e32 v83, v83
	v_cvt_pk_f16_f32 v148, v76, v77
	v_pk_add_f16 v0, v0, v118
	v_pk_add_f16 v72, v92, v119
	v_cvt_pk_f16_f32 v149, v78, v79
	ds_read_b64_tr_b16 v[64:65], v211 offset:64512
	ds_read_b64_tr_b16 v[66:67], v211 offset:65024
	v_mfma_f32_32x32x16_bf16 v[36:51], v[156:159], v[132:135], v[36:51]
	v_pk_add_f16 v0, v0, v148
	v_pk_add_f16 v170, v72, v149
	v_cvt_pk_f16_f32 v150, v80, v81
	v_cvt_pk_f16_f32 v151, v82, v83
	s_add_u32 s62, s56, 0x54000
	s_addc_u32 s63, s57, 0
	s_mov_b32 m0, s71
	s_nop 0
	global_load_lds_dwordx4 v165, s[62:63]
	s_add_u32 s62, s58, 0x3c000
	s_addc_u32 s63, s59, 0
	s_add_i32 s60, s60, 0x16000
	s_mov_b32 m0, s60
	s_nop 0
	global_load_lds_dwordx4 v164, s[62:63]
	s_waitcnt lgkmcnt(14)
	v_mfma_f32_32x32x16_f16 v[4:19], v[124:127], v[160:163], v[4:19]
	v_exp_f32_e32 v100, v100
	v_exp_f32_e32 v101, v101
	v_exp_f32_e32 v102, v102
	s_waitcnt lgkmcnt(12)
	v_mfma_f32_32x32x16_f16 v[20:35], v[124:127], v[84:87], v[20:35]
	v_exp_f32_e32 v103, v103
	v_exp_f32_e32 v104, v104
	v_exp_f32_e32 v105, v105
	ds_read_b128 v[92:95], v210 offset:24576
	ds_read_b128 v[96:99], v210 offset:26624
	s_waitcnt lgkmcnt(12)
	v_mfma_f32_32x32x16_f16 v[4:19], v[120:123], v[52:55], v[4:19]
	v_exp_f32_e32 v106, v106
	v_exp_f32_e32 v107, v107
	v_exp_f32_e32 v108, v108
	ds_read_b128 v[144:147], v210 offset:25088
	ds_read_b128 v[152:155], v210 offset:27136
	s_waitcnt lgkmcnt(12)
	v_mfma_f32_32x32x16_f16 v[20:35], v[120:123], v[56:59], v[20:35]
	v_exp_f32_e32 v109, v109
	v_exp_f32_e32 v110, v110
	v_exp_f32_e32 v111, v111
	ds_read_b128 v[156:159], v210 offset:28672
	ds_read_b128 v[160:163], v210 offset:30720
	s_waitcnt lgkmcnt(12)
	v_mfma_f32_32x32x16_f16 v[4:19], v[116:119], v[88:91], v[4:19]
	v_exp_f32_e32 v112, v112
	v_exp_f32_e32 v113, v113
	v_exp_f32_e32 v114, v114
	ds_read_b128 v[88:91], v210 offset:29184
	ds_read_b128 v[84:87], v210 offset:31232
	s_waitcnt lgkmcnt(12)
	v_mfma_f32_32x32x16_f16 v[20:35], v[116:119], v[60:63], v[20:35]
	v_exp_f32_e32 v115, v115
	v_exp_f32_e32 v36, v36
	v_exp_f32_e32 v37, v37
	s_waitcnt lgkmcnt(10)
	v_mfma_f32_32x32x16_f16 v[4:19], v[148:151], v[68:71], v[4:19]
	v_exp_f32_e32 v38, v38
	v_exp_f32_e32 v39, v39
	v_exp_f32_e32 v40, v40
	s_waitcnt lgkmcnt(8)
	v_mfma_f32_32x32x16_f16 v[20:35], v[148:151], v[64:67], v[20:35]
	v_exp_f32_e32 v41, v41
	v_exp_f32_e32 v42, v42
	v_exp_f32_e32 v43, v43
	s_waitcnt vmcnt(4) lgkmcnt(0)
	s_barrier
	ds_read_b64_tr_b16 v[166:167], v212 offset:16384
	ds_read_b64_tr_b16 v[168:169], v212 offset:16896
	s_waitcnt lgkmcnt(9)
	v_mfma_f32_32x32x16_bf16 v[68:83], v[92:95], v[140:143], -4.0
	v_cvt_pk_f16_f32 v124, v100, v101
	v_pk_add_f16 v0, v0, v150
	v_pk_add_f16 v52, v170, v151
	v_pk_add_f16 v0, v0, v52
	v_cvt_pk_f16_f32 v125, v102, v103
	v_dot2c_f32_f16_e32 v2, 0x3c003c00, v0
	ds_read_b64_tr_b16 v[92:93], v212 offset:20480
	ds_read_b64_tr_b16 v[94:95], v212 offset:20992
	s_waitcnt lgkmcnt(10)
	v_mfma_f32_32x32x16_bf16 v[52:67], v[96:99], v[140:143], -4.0
	v_exp_f32_e32 v44, v44
	v_cvt_pk_f16_f32 v126, v104, v105
	v_cvt_pk_f16_f32 v127, v106, v107
	ds_read_b64_tr_b16 v[96:97], v212 offset:17408
	ds_read_b64_tr_b16 v[98:99], v212 offset:17920
	s_waitcnt lgkmcnt(11)
	v_mfma_f32_32x32x16_bf16 v[68:83], v[144:147], v[128:131], v[68:83]
	v_exp_f32_e32 v45, v45
	v_cvt_pk_f16_f32 v120, v108, v109
	v_pk_add_f16 v0, v124, v126
	v_pk_add_f16 v104, v125, v127
	v_cvt_pk_f16_f32 v121, v110, v111
	ds_read_b64_tr_b16 v[100:101], v212 offset:21504
	ds_read_b64_tr_b16 v[102:103], v212 offset:22016
	s_waitcnt lgkmcnt(12)
	v_mfma_f32_32x32x16_bf16 v[52:67], v[152:155], v[128:131], v[52:67]
	v_exp_f32_e32 v46, v46
	v_exp_f32_e32 v47, v47
	v_pk_add_f16 v0, v0, v120
	v_pk_add_f16 v108, v104, v121
	v_cvt_pk_f16_f32 v122, v112, v113
	v_cvt_pk_f16_f32 v123, v114, v115
	ds_read_b64_tr_b16 v[104:105], v212 offset:18432
	ds_read_b64_tr_b16 v[106:107], v212 offset:18944
	s_waitcnt lgkmcnt(13)
	v_mfma_f32_32x32x16_bf16 v[68:83], v[156:159], v[136:139], v[68:83]
	v_exp_f32_e32 v48, v48
	v_exp_f32_e32 v49, v49
	v_cvt_pk_f16_f32 v116, v36, v37
	v_pk_add_f16 v0, v0, v122
	v_pk_add_f16 v108, v108, v123
	v_cvt_pk_f16_f32 v117, v38, v39
	ds_read_b64_tr_b16 v[36:37], v212 offset:22528
	ds_read_b64_tr_b16 v[38:39], v212 offset:23040
	s_waitcnt lgkmcnt(14)
	v_mfma_f32_32x32x16_bf16 v[52:67], v[160:163], v[136:139], v[52:67]
	v_exp_f32_e32 v50, v50
	v_pk_add_f16 v0, v0, v116
	v_pk_add_f16 v108, v108, v117
	v_cvt_pk_f16_f32 v118, v40, v41
	v_cvt_pk_f16_f32 v119, v42, v43
	ds_read_b64_tr_b16 v[40:41], v212 offset:19456
	ds_read_b64_tr_b16 v[42:43], v212 offset:19968
	s_waitcnt lgkmcnt(14)
	v_mfma_f32_32x32x16_bf16 v[68:83], v[88:91], v[132:135], v[68:83]
	v_exp_f32_e32 v51, v51
	v_cvt_pk_f16_f32 v148, v44, v45
	v_pk_add_f16 v0, v0, v118
	v_pk_add_f16 v88, v108, v119
	v_cvt_pk_f16_f32 v149, v46, v47
	ds_read_b64_tr_b16 v[44:45], v212 offset:23552
	ds_read_b64_tr_b16 v[46:47], v212 offset:24064
	v_mfma_f32_32x32x16_bf16 v[52:67], v[84:87], v[132:135], v[52:67]
	v_pk_add_f16 v0, v0, v148
	v_pk_add_f16 v170, v88, v149
	v_cvt_pk_f16_f32 v150, v48, v49
	v_cvt_pk_f16_f32 v151, v50, v51
	s_add_u32 s60, s56, 0x60000
	s_addc_u32 s61, s57, 0
	s_mov_b32 m0, s76
	s_nop 0
	global_load_lds_dwordx4 v165, s[60:61]
	s_add_u32 s60, s58, 0x48000
	s_addc_u32 s61, s59, 0
	s_mov_b32 m0, s10
	s_nop 0
	global_load_lds_dwordx4 v164, s[60:61]
	s_waitcnt lgkmcnt(14)
	v_mfma_f32_32x32x16_f16 v[4:19], v[124:127], v[166:169], v[4:19]
	v_exp_f32_e32 v68, v68
	v_exp_f32_e32 v69, v69
	v_exp_f32_e32 v70, v70
	s_waitcnt lgkmcnt(12)
	v_mfma_f32_32x32x16_f16 v[20:35], v[124:127], v[92:95], v[20:35]
	v_exp_f32_e32 v71, v71
	v_exp_f32_e32 v72, v72
	v_exp_f32_e32 v73, v73
	ds_read_b128 v[48:51], v210 offset:32768
	ds_read_b128 v[84:87], v210 offset:34816
	s_waitcnt lgkmcnt(12)
	v_mfma_f32_32x32x16_f16 v[4:19], v[120:123], v[96:99], v[4:19]
	v_exp_f32_e32 v74, v74
	v_exp_f32_e32 v75, v75
	v_exp_f32_e32 v76, v76
	ds_read_b128 v[88:91], v210 offset:33280
	ds_read_b128 v[92:95], v210 offset:35328
	s_waitcnt lgkmcnt(12)
	v_mfma_f32_32x32x16_f16 v[20:35], v[120:123], v[100:103], v[20:35]
	v_exp_f32_e32 v77, v77
	v_exp_f32_e32 v78, v78
	v_exp_f32_e32 v79, v79
	ds_read_b128 v[96:99], v210 offset:36864
	ds_read_b128 v[144:147], v210 offset:38912
	s_waitcnt lgkmcnt(12)
	v_mfma_f32_32x32x16_f16 v[4:19], v[116:119], v[104:107], v[4:19]
	v_exp_f32_e32 v80, v80
	v_exp_f32_e32 v81, v81
	v_exp_f32_e32 v82, v82
	ds_read_b128 v[152:155], v210 offset:37376
	ds_read_b128 v[156:159], v210 offset:39424
	s_waitcnt lgkmcnt(12)
	v_mfma_f32_32x32x16_f16 v[20:35], v[116:119], v[36:39], v[20:35]
	v_exp_f32_e32 v83, v83
	v_exp_f32_e32 v52, v52
	v_exp_f32_e32 v53, v53
	s_waitcnt lgkmcnt(10)
	v_mfma_f32_32x32x16_f16 v[4:19], v[148:151], v[40:43], v[4:19]
	v_exp_f32_e32 v54, v54
	v_exp_f32_e32 v55, v55
	v_exp_f32_e32 v56, v56
	s_waitcnt lgkmcnt(8)
	v_mfma_f32_32x32x16_f16 v[20:35], v[148:151], v[44:47], v[20:35]
	v_exp_f32_e32 v57, v57
	v_exp_f32_e32 v58, v58
	v_exp_f32_e32 v59, v59
	ds_read_b64_tr_b16 v[160:161], v212 offset:24576
	ds_read_b64_tr_b16 v[162:163], v212 offset:25088
	s_waitcnt lgkmcnt(9)
	v_mfma_f32_32x32x16_bf16 v[100:115], v[48:51], v[140:143], -4.0
	v_exp_f32_e32 v60, v60
	v_cvt_pk_f16_f32 v124, v68, v69
	v_pk_add_f16 v0, v0, v150
	v_pk_add_f16 v116, v170, v151
	v_cvt_pk_f16_f32 v125, v70, v71
	ds_read_b64_tr_b16 v[68:69], v212 offset:28672
	ds_read_b64_tr_b16 v[70:71], v212 offset:29184
	s_waitcnt lgkmcnt(10)
	v_mfma_f32_32x32x16_bf16 v[36:51], v[84:87], v[140:143], -4.0
	v_exp_f32_e32 v61, v61
	v_pk_add_f16 v0, v0, v124
	v_pk_add_f16 v84, v116, v125
	v_cvt_pk_f16_f32 v126, v72, v73
	v_cvt_pk_f16_f32 v127, v74, v75
	ds_read_b64_tr_b16 v[72:73], v212 offset:25600
	ds_read_b64_tr_b16 v[74:75], v212 offset:26112
	s_waitcnt lgkmcnt(11)
	v_mfma_f32_32x32x16_bf16 v[100:115], v[88:91], v[128:131], v[100:115]
	v_exp_f32_e32 v62, v62
	v_cvt_pk_f16_f32 v120, v76, v77
	v_pk_add_f16 v0, v0, v126
	v_pk_add_f16 v84, v84, v127
	v_cvt_pk_f16_f32 v121, v78, v79
	ds_read_b64_tr_b16 v[76:77], v212 offset:29696
	ds_read_b64_tr_b16 v[78:79], v212 offset:30208
	s_waitcnt lgkmcnt(12)
	v_mfma_f32_32x32x16_bf16 v[36:51], v[92:95], v[128:131], v[36:51]
	v_exp_f32_e32 v63, v63
	v_exp_f32_e32 v64, v64
	v_pk_add_f16 v0, v0, v120
	v_pk_add_f16 v84, v84, v121
	v_cvt_pk_f16_f32 v122, v80, v81
	v_cvt_pk_f16_f32 v123, v82, v83
	ds_read_b64_tr_b16 v[80:81], v212 offset:26624
	ds_read_b64_tr_b16 v[82:83], v212 offset:27136
	s_waitcnt lgkmcnt(13)
	v_mfma_f32_32x32x16_bf16 v[100:115], v[96:99], v[136:139], v[100:115]
	v_exp_f32_e32 v65, v65
	v_cvt_pk_f16_f32 v116, v52, v53
	v_pk_add_f16 v0, v0, v122
	v_pk_add_f16 v88, v84, v123
	v_cvt_pk_f16_f32 v117, v54, v55
	ds_read_b64_tr_b16 v[84:85], v212 offset:30720
	ds_read_b64_tr_b16 v[86:87], v212 offset:31232
	s_waitcnt lgkmcnt(14)
	v_mfma_f32_32x32x16_bf16 v[36:51], v[144:147], v[136:139], v[36:51]
	v_exp_f32_e32 v66, v66
	v_pk_add_f16 v0, v0, v116
	v_pk_add_f16 v52, v88, v117
	v_cvt_pk_f16_f32 v118, v56, v57
	v_cvt_pk_f16_f32 v119, v58, v59
	ds_read_b64_tr_b16 v[56:57], v212 offset:27648
	ds_read_b64_tr_b16 v[58:59], v212 offset:28160
	s_waitcnt lgkmcnt(14)
	v_mfma_f32_32x32x16_bf16 v[100:115], v[152:155], v[132:135], v[100:115]
	v_exp_f32_e32 v67, v67
	v_cvt_pk_f16_f32 v148, v60, v61
	v_pk_add_f16 v0, v0, v118
	v_pk_add_f16 v52, v52, v119
	v_cvt_pk_f16_f32 v149, v62, v63
	ds_read_b64_tr_b16 v[60:61], v212 offset:31744
	ds_read_b64_tr_b16 v[62:63], v212 offset:32256
	v_mfma_f32_32x32x16_bf16 v[36:51], v[156:159], v[132:135], v[36:51]
	v_pk_add_f16 v0, v0, v148
	v_pk_add_f16 v174, v52, v149
	v_cvt_pk_f16_f32 v150, v64, v65
	v_cvt_pk_f16_f32 v151, v66, v67
	s_add_u32 s60, s56, 0x6c000
	s_addc_u32 s61, s57, 0
	s_mov_b32 m0, s77
	s_nop 0
	global_load_lds_dwordx4 v165, s[60:61]
	s_add_u32 s60, s58, 0x54000
	s_addc_u32 s61, s59, 0
	s_mov_b32 m0, s78
	s_nop 0
	global_load_lds_dwordx4 v164, s[60:61]
	s_waitcnt lgkmcnt(14)
	v_mfma_f32_32x32x16_f16 v[4:19], v[124:127], v[160:163], v[4:19]
	v_exp_f32_e32 v100, v100
	v_exp_f32_e32 v101, v101
	v_exp_f32_e32 v102, v102
	s_waitcnt lgkmcnt(12)
	v_mfma_f32_32x32x16_f16 v[20:35], v[124:127], v[68:71], v[20:35]
	v_exp_f32_e32 v103, v103
	v_exp_f32_e32 v104, v104
	v_exp_f32_e32 v105, v105
	ds_read_b128 v[64:67], v210 offset:40960
	ds_read_b128 v[144:147], v210 offset:43008
	s_waitcnt lgkmcnt(12)
	v_mfma_f32_32x32x16_f16 v[4:19], v[120:123], v[72:75], v[4:19]
	v_exp_f32_e32 v106, v106
	v_exp_f32_e32 v107, v107
	v_exp_f32_e32 v108, v108
	ds_read_b128 v[152:155], v210 offset:41472
	ds_read_b128 v[156:159], v210 offset:43520
	s_waitcnt lgkmcnt(12)
	v_mfma_f32_32x32x16_f16 v[20:35], v[120:123], v[76:79], v[20:35]
	v_exp_f32_e32 v109, v109
	v_exp_f32_e32 v110, v110
	v_exp_f32_e32 v111, v111
	ds_read_b128 v[160:163], v210 offset:45056
	ds_read_b128 v[166:169], v210 offset:47104
	s_waitcnt lgkmcnt(12)
	v_mfma_f32_32x32x16_f16 v[4:19], v[116:119], v[80:83], v[4:19]
	v_exp_f32_e32 v112, v112
	v_exp_f32_e32 v113, v113
	v_exp_f32_e32 v114, v114
	ds_read_b128 v[170:173], v210 offset:45568
	ds_read_b128 v[52:55], v210 offset:47616
	s_waitcnt lgkmcnt(12)
	v_mfma_f32_32x32x16_f16 v[20:35], v[116:119], v[84:87], v[20:35]
	v_exp_f32_e32 v115, v115
	v_exp_f32_e32 v36, v36
	v_exp_f32_e32 v37, v37
	s_waitcnt lgkmcnt(10)
	v_mfma_f32_32x32x16_f16 v[4:19], v[148:151], v[56:59], v[4:19]
	v_exp_f32_e32 v38, v38
	v_exp_f32_e32 v39, v39
	v_exp_f32_e32 v40, v40
	s_waitcnt lgkmcnt(8)
	v_mfma_f32_32x32x16_f16 v[20:35], v[148:151], v[60:63], v[20:35]
	v_exp_f32_e32 v41, v41
	v_exp_f32_e32 v42, v42
	v_exp_f32_e32 v43, v43
	s_waitcnt vmcnt(4) lgkmcnt(0)
	s_barrier
	ds_read_b64_tr_b16 v[56:57], v212 offset:32768
	ds_read_b64_tr_b16 v[58:59], v212 offset:33280
	s_waitcnt lgkmcnt(9)
	v_mfma_f32_32x32x16_bf16 v[84:99], v[64:67], v[140:143], -4.0
	v_pk_add_f16 v0, v0, v150
	v_pk_add_f16 v60, v174, v151
	v_cvt_pk_f16_f32 v124, v100, v101
	v_pk_add_f16 v0, v0, v60
	v_cvt_pk_f16_f32 v125, v102, v103
	v_dot2c_f32_f16_e32 v2, 0x3c003c00, v0
	ds_read_b64_tr_b16 v[60:61], v212 offset:36864
	ds_read_b64_tr_b16 v[62:63], v212 offset:37376
	s_waitcnt lgkmcnt(10)
	v_mfma_f32_32x32x16_bf16 v[68:83], v[144:147], v[140:143], -4.0
	v_exp_f32_e32 v44, v44
	v_cvt_pk_f16_f32 v126, v104, v105
	v_cvt_pk_f16_f32 v127, v106, v107
	ds_read_b64_tr_b16 v[64:65], v212 offset:33792
	ds_read_b64_tr_b16 v[66:67], v212 offset:34304
	s_waitcnt lgkmcnt(11)
	v_mfma_f32_32x32x16_bf16 v[84:99], v[152:155], v[128:131], v[84:99]
	v_exp_f32_e32 v45, v45
	v_pk_add_f16 v0, v124, v126
	v_pk_add_f16 v104, v125, v127
	v_cvt_pk_f16_f32 v120, v108, v109
	v_cvt_pk_f16_f32 v121, v110, v111
	ds_read_b64_tr_b16 v[100:101], v212 offset:37888
	ds_read_b64_tr_b16 v[102:103], v212 offset:38400
	s_waitcnt lgkmcnt(12)
	v_mfma_f32_32x32x16_bf16 v[68:83], v[156:159], v[128:131], v[68:83]
	v_exp_f32_e32 v46, v46
	v_exp_f32_e32 v47, v47
	v_pk_add_f16 v0, v0, v120
	v_pk_add_f16 v108, v104, v121
	v_cvt_pk_f16_f32 v122, v112, v113
	v_cvt_pk_f16_f32 v123, v114, v115
	ds_read_b64_tr_b16 v[104:105], v212 offset:34816
	ds_read_b64_tr_b16 v[106:107], v212 offset:35328
	s_waitcnt lgkmcnt(13)
	v_mfma_f32_32x32x16_bf16 v[84:99], v[160:163], v[136:139], v[84:99]
	v_exp_f32_e32 v48, v48
	v_exp_f32_e32 v49, v49
	v_pk_add_f16 v0, v0, v122
	v_pk_add_f16 v108, v108, v123
	v_cvt_pk_f16_f32 v116, v36, v37
	v_cvt_pk_f16_f32 v117, v38, v39
	ds_read_b64_tr_b16 v[36:37], v212 offset:38912
	ds_read_b64_tr_b16 v[38:39], v212 offset:39424
	s_waitcnt lgkmcnt(14)
	v_mfma_f32_32x32x16_bf16 v[68:83], v[166:169], v[136:139], v[68:83]
	v_exp_f32_e32 v50, v50
	v_pk_add_f16 v0, v0, v116
	v_pk_add_f16 v108, v108, v117
	v_cvt_pk_f16_f32 v118, v40, v41
	v_cvt_pk_f16_f32 v119, v42, v43
	ds_read_b64_tr_b16 v[40:41], v212 offset:35840
	ds_read_b64_tr_b16 v[42:43], v212 offset:36352
	v_cvt_pk_f16_f32 v148, v44, v45
	v_pk_add_f16 v0, v0, v118
	v_pk_add_f16 v108, v108, v119
	v_cvt_pk_f16_f32 v149, v46, v47
	s_waitcnt lgkmcnt(14)
	v_mfma_f32_32x32x16_bf16 v[84:99], v[170:173], v[132:135], v[84:99]
	v_exp_f32_e32 v51, v51
	ds_read_b64_tr_b16 v[44:45], v212 offset:39936
	ds_read_b64_tr_b16 v[46:47], v212 offset:40448
	v_mfma_f32_32x32x16_bf16 v[68:83], v[52:55], v[132:135], v[68:83]
	v_pk_add_f16 v0, v0, v148
	v_pk_add_f16 v166, v108, v149
	v_cvt_pk_f16_f32 v150, v48, v49
	v_cvt_pk_f16_f32 v151, v50, v51
	s_add_u32 s60, s56, 0x78000
	s_addc_u32 s61, s57, 0
	s_mov_b32 m0, s79
	s_nop 0
	global_load_lds_dwordx4 v165, s[60:61]
	s_add_u32 s60, s58, 0x60000
	s_addc_u32 s61, s59, 0
	s_mov_b32 m0, s92
	s_nop 0
	global_load_lds_dwordx4 v164, s[60:61]
	s_waitcnt lgkmcnt(14)
	v_mfma_f32_32x32x16_f16 v[4:19], v[124:127], v[56:59], v[4:19]
	v_exp_f32_e32 v84, v84
	v_exp_f32_e32 v85, v85
	v_exp_f32_e32 v86, v86
	s_waitcnt lgkmcnt(12)
	v_mfma_f32_32x32x16_f16 v[20:35], v[124:127], v[60:63], v[20:35]
	v_exp_f32_e32 v87, v87
	v_exp_f32_e32 v88, v88
	v_exp_f32_e32 v89, v89
	ds_read_b128 v[48:51], v210
	ds_read_b128 v[108:111], v210 offset:2048
	s_waitcnt lgkmcnt(12)
	v_mfma_f32_32x32x16_f16 v[4:19], v[120:123], v[64:67], v[4:19]
	v_exp_f32_e32 v90, v90
	v_exp_f32_e32 v91, v91
	v_exp_f32_e32 v92, v92
	ds_read_b128 v[112:115], v210 offset:512
	ds_read_b128 v[144:147], v210 offset:2560
	s_waitcnt lgkmcnt(12)
	v_mfma_f32_32x32x16_f16 v[20:35], v[120:123], v[100:103], v[20:35]
	v_exp_f32_e32 v93, v93
	v_exp_f32_e32 v94, v94
	v_exp_f32_e32 v95, v95
	ds_read_b128 v[100:103], v210 offset:4096
	ds_read_b128 v[152:155], v210 offset:6144
	s_waitcnt lgkmcnt(12)
	v_mfma_f32_32x32x16_f16 v[4:19], v[116:119], v[104:107], v[4:19]
	v_exp_f32_e32 v96, v96
	v_exp_f32_e32 v97, v97
	v_exp_f32_e32 v98, v98
	ds_read_b128 v[104:107], v210 offset:4608
	ds_read_b128 v[156:159], v210 offset:6656
	s_waitcnt lgkmcnt(12)
	v_mfma_f32_32x32x16_f16 v[20:35], v[116:119], v[36:39], v[20:35]
	v_exp_f32_e32 v99, v99
	v_exp_f32_e32 v68, v68
	v_exp_f32_e32 v69, v69
	s_waitcnt lgkmcnt(10)
	v_mfma_f32_32x32x16_f16 v[4:19], v[148:151], v[40:43], v[4:19]
	v_exp_f32_e32 v70, v70
	v_exp_f32_e32 v71, v71
	v_exp_f32_e32 v72, v72
	s_waitcnt lgkmcnt(8)
	v_mfma_f32_32x32x16_f16 v[20:35], v[148:151], v[44:47], v[20:35]
	v_exp_f32_e32 v73, v73
	v_exp_f32_e32 v74, v74
	v_exp_f32_e32 v75, v75
	ds_read_b64_tr_b16 v[160:161], v212 offset:40960
	ds_read_b64_tr_b16 v[162:163], v212 offset:41472
	s_waitcnt lgkmcnt(9)
	v_mfma_f32_32x32x16_bf16 v[52:67], v[48:51], v[140:143], -4.0
	v_exp_f32_e32 v76, v76
	v_cvt_pk_f16_f32 v124, v84, v85
	v_pk_add_f16 v0, v0, v150
	v_pk_add_f16 v116, v166, v151
	v_cvt_pk_f16_f32 v125, v86, v87
	ds_read_b64_tr_b16 v[84:85], v212 offset:45056
	ds_read_b64_tr_b16 v[86:87], v212 offset:45568
	s_waitcnt lgkmcnt(10)
	v_mfma_f32_32x32x16_bf16 v[36:51], v[108:111], v[140:143], -4.0
	v_exp_f32_e32 v77, v77
	v_pk_add_f16 v0, v0, v124
	v_pk_add_f16 v108, v116, v125
	v_cvt_pk_f16_f32 v126, v88, v89
	v_cvt_pk_f16_f32 v127, v90, v91
	ds_read_b64_tr_b16 v[88:89], v212 offset:41984
	ds_read_b64_tr_b16 v[90:91], v212 offset:42496
	s_waitcnt lgkmcnt(11)
	v_mfma_f32_32x32x16_bf16 v[52:67], v[112:115], v[128:131], v[52:67]
	v_exp_f32_e32 v78, v78
	v_cvt_pk_f16_f32 v120, v92, v93
	v_pk_add_f16 v0, v0, v126
	v_pk_add_f16 v108, v108, v127
	v_cvt_pk_f16_f32 v121, v94, v95
	ds_read_b64_tr_b16 v[92:93], v212 offset:46080
	ds_read_b64_tr_b16 v[94:95], v212 offset:46592
	s_waitcnt lgkmcnt(12)
	v_mfma_f32_32x32x16_bf16 v[36:51], v[144:147], v[128:131], v[36:51]
	v_exp_f32_e32 v79, v79
	v_exp_f32_e32 v80, v80
	v_pk_add_f16 v0, v0, v120
	v_pk_add_f16 v108, v108, v121
	v_cvt_pk_f16_f32 v122, v96, v97
	v_cvt_pk_f16_f32 v123, v98, v99
	ds_read_b64_tr_b16 v[96:97], v212 offset:43008
	ds_read_b64_tr_b16 v[98:99], v212 offset:43520
	s_waitcnt lgkmcnt(13)
	v_mfma_f32_32x32x16_bf16 v[52:67], v[100:103], v[136:139], v[52:67]
	v_exp_f32_e32 v81, v81
	v_cvt_pk_f16_f32 v116, v68, v69
	v_pk_add_f16 v0, v0, v122
	v_pk_add_f16 v100, v108, v123
	v_cvt_pk_f16_f32 v117, v70, v71
	ds_read_b64_tr_b16 v[166:167], v212 offset:47104
	ds_read_b64_tr_b16 v[168:169], v212 offset:47616
	s_waitcnt lgkmcnt(14)
	v_mfma_f32_32x32x16_bf16 v[36:51], v[152:155], v[136:139], v[36:51]
	v_exp_f32_e32 v82, v82
	v_pk_add_f16 v0, v0, v116
	v_pk_add_f16 v68, v100, v117
	v_cvt_pk_f16_f32 v118, v72, v73
	v_cvt_pk_f16_f32 v119, v74, v75
	ds_read_b64_tr_b16 v[170:171], v212 offset:44032
	ds_read_b64_tr_b16 v[172:173], v212 offset:44544
	s_waitcnt lgkmcnt(14)
	v_mfma_f32_32x32x16_bf16 v[52:67], v[104:107], v[132:135], v[52:67]
	v_exp_f32_e32 v83, v83
	v_cvt_pk_f16_f32 v148, v76, v77
	v_pk_add_f16 v0, v0, v118
	v_pk_add_f16 v68, v68, v119
	v_cvt_pk_f16_f32 v149, v78, v79
	ds_read_b64_tr_b16 v[74:75], v212 offset:48128
	ds_read_b64_tr_b16 v[76:77], v212 offset:48640
	v_mfma_f32_32x32x16_bf16 v[36:51], v[156:159], v[132:135], v[36:51]
	v_cvt_pk_f16_f32 v150, v80, v81
	v_mov_b64_e32 v[144:145], v[148:149]
	v_pk_add_f16 v72, v0, v148
	v_cvt_pk_f16_f32 v0, v82, v83
	v_mov_b64_e32 v[146:147], v[150:151]
	v_pk_add_f16 v73, v68, v149
	v_mov_b32_e32 v147, v0
	s_add_u32 s56, s56, 0x84000
	s_addc_u32 s57, s57, 0
	s_mov_b32 m0, s85
	s_nop 0
	global_load_lds_dwordx4 v165, s[56:57]
	s_add_u32 s56, s58, 0x6c000
	s_addc_u32 s57, s59, 0
	s_mov_b32 m0, s93
	s_nop 0
	global_load_lds_dwordx4 v164, s[56:57]
	s_waitcnt lgkmcnt(14)
	v_mfma_f32_32x32x16_f16 v[4:19], v[124:127], v[160:163], v[4:19]
	v_exp_f32_e32 v52, v52
	v_exp_f32_e32 v53, v53
	v_exp_f32_e32 v54, v54
	s_waitcnt lgkmcnt(12)
	v_mfma_f32_32x32x16_f16 v[20:35], v[124:127], v[84:87], v[20:35]
	v_exp_f32_e32 v55, v55
	v_exp_f32_e32 v56, v56
	v_exp_f32_e32 v57, v57
	ds_read_b128 v[68:71], v210 offset:8192
	ds_read_b128 v[160:163], v210 offset:10240
	s_waitcnt lgkmcnt(12)
	v_mfma_f32_32x32x16_f16 v[4:19], v[120:123], v[88:91], v[4:19]
	v_exp_f32_e32 v58, v58
	v_exp_f32_e32 v59, v59
	v_exp_f32_e32 v60, v60
	ds_read_b128 v[156:159], v210 offset:8704
	ds_read_b128 v[112:115], v210 offset:10752
	s_waitcnt lgkmcnt(12)
	v_mfma_f32_32x32x16_f16 v[20:35], v[120:123], v[92:95], v[20:35]
	v_exp_f32_e32 v61, v61
	v_exp_f32_e32 v62, v62
	v_exp_f32_e32 v63, v63
	ds_read_b128 v[152:155], v210 offset:12288
	ds_read_b128 v[104:107], v210 offset:14336
	s_waitcnt lgkmcnt(12)
	v_mfma_f32_32x32x16_f16 v[4:19], v[116:119], v[96:99], v[4:19]
	v_exp_f32_e32 v64, v64
	v_exp_f32_e32 v65, v65
	v_exp_f32_e32 v66, v66
	ds_read_b128 v[108:111], v210 offset:12800
	ds_read_b128 v[100:103], v210 offset:14848
	s_waitcnt lgkmcnt(12)
	v_mfma_f32_32x32x16_f16 v[20:35], v[116:119], v[166:169], v[20:35]
	v_exp_f32_e32 v67, v67
	v_exp_f32_e32 v36, v36
	v_exp_f32_e32 v37, v37
	s_waitcnt lgkmcnt(10)
	v_mfma_f32_32x32x16_f16 v[4:19], v[144:147], v[170:173], v[4:19]
	v_exp_f32_e32 v38, v38
	v_exp_f32_e32 v39, v39
	v_exp_f32_e32 v40, v40
	s_waitcnt lgkmcnt(8)
	v_mfma_f32_32x32x16_f16 v[20:35], v[144:147], v[74:77], v[20:35]
	v_exp_f32_e32 v41, v41
	v_exp_f32_e32 v42, v42
	v_exp_f32_e32 v43, v43
	s_add_i32 s53, s53, 6
	s_add_u32 s54, s54, 0x48000
	s_addc_u32 s55, s55, 0
	v_mov_b32_e32 v151, v0
	s_cmpk_gt_u32 s53, 0xef
	s_waitcnt vmcnt(4) lgkmcnt(0)
	s_barrier
	s_cbranch_scc0 .LBB0_336
	v_exp_f32_e32 v44, v44
	v_exp_f32_e32 v45, v45
	v_exp_f32_e32 v46, v46
	v_exp_f32_e32 v47, v47
	v_exp_f32_e32 v48, v48
	v_exp_f32_e32 v49, v49
	v_exp_f32_e32 v50, v50
	v_exp_f32_e32 v51, v51
	s_and_b32 s11, s11, 0x3fffffc0
	s_lshl_b32 s11, s11, 2
	s_add_i32 s11, s11, 0
	s_add_i32 s11, s11, 0x18000
	ds_read_b64_tr_b16 v[148:149], v211 offset:49152
	ds_read_b64_tr_b16 v[150:151], v211 offset:49664
	s_waitcnt lgkmcnt(9)
	v_mfma_f32_32x32x16_bf16 v[84:99], v[68:71], v[140:143], -4.0
	v_mov_b32_e32 v116, v3
	v_pk_add_f16 v0, v72, v146
	v_pk_add_f16 v68, v73, v147
	v_cvt_pk_f16_f32 v124, v52, v53
	v_pk_add_f16 v0, v0, v68
	v_cvt_pk_f16_f32 v125, v54, v55
	v_dot2c_f32_f16_e32 v2, 0x3c003c00, v0
	v_mov_b32_e32 v0, v3
	ds_read_b64_tr_b16 v[52:53], v211 offset:53248
	ds_read_b64_tr_b16 v[54:55], v211 offset:53760
	s_waitcnt lgkmcnt(10)
	v_mfma_f32_32x32x16_bf16 v[68:83], v[160:163], v[140:143], -4.0
	s_nop 0
	v_pk_add_f16 v0, v0, v124
	v_pk_add_f16 v116, v116, v125
	v_cvt_pk_f16_f32 v126, v56, v57
	v_cvt_pk_f16_f32 v127, v58, v59
	ds_read_b64_tr_b16 v[56:57], v211 offset:50176
	ds_read_b64_tr_b16 v[58:59], v211 offset:50688
	s_waitcnt lgkmcnt(11)
	v_mfma_f32_32x32x16_bf16 v[84:99], v[156:159], v[128:131], v[84:99]
	v_pk_add_f16 v0, v0, v126
	v_pk_add_f16 v116, v116, v127
	v_cvt_pk_f16_f32 v120, v60, v61
	v_cvt_pk_f16_f32 v121, v62, v63
	ds_read_b64_tr_b16 v[60:61], v211 offset:54272
	ds_read_b64_tr_b16 v[62:63], v211 offset:54784
	s_waitcnt lgkmcnt(12)
	v_mfma_f32_32x32x16_bf16 v[68:83], v[112:115], v[128:131], v[68:83]
	v_pk_add_f16 v0, v0, v120
	v_pk_add_f16 v116, v116, v121
	v_cvt_pk_f16_f32 v122, v64, v65
	v_cvt_pk_f16_f32 v123, v66, v67
	ds_read_b64_tr_b16 v[64:65], v211 offset:51200
	ds_read_b64_tr_b16 v[66:67], v211 offset:51712
	s_waitcnt lgkmcnt(13)
	v_mfma_f32_32x32x16_bf16 v[84:99], v[152:155], v[136:139], v[84:99]
	v_pk_add_f16 v0, v0, v122
	v_pk_add_f16 v112, v116, v123
	v_cvt_pk_f16_f32 v116, v36, v37
	v_cvt_pk_f16_f32 v117, v38, v39
	ds_read_b64_tr_b16 v[36:37], v211 offset:55296
	ds_read_b64_tr_b16 v[38:39], v211 offset:55808
	s_waitcnt lgkmcnt(14)
	v_mfma_f32_32x32x16_bf16 v[68:83], v[104:107], v[136:139], v[68:83]
	v_pk_add_f16 v0, v0, v116
	v_pk_add_f16 v112, v112, v117
	v_cvt_pk_f16_f32 v118, v40, v41
	v_cvt_pk_f16_f32 v119, v42, v43
	ds_read_b64_tr_b16 v[40:41], v211 offset:52224
	ds_read_b64_tr_b16 v[42:43], v211 offset:52736
	s_waitcnt lgkmcnt(14)
	v_mfma_f32_32x32x16_bf16 v[84:99], v[108:111], v[132:135], v[84:99]
	v_pk_add_f16 v0, v0, v118
	v_pk_add_f16 v104, v112, v119
	v_cvt_pk_f16_f32 v144, v44, v45
	v_cvt_pk_f16_f32 v145, v46, v47
	ds_read_b64_tr_b16 v[44:45], v211 offset:56320
	ds_read_b64_tr_b16 v[46:47], v211 offset:56832
	v_mfma_f32_32x32x16_bf16 v[68:83], v[100:103], v[132:135], v[68:83]
	v_pk_add_f16 v0, v0, v144
	v_pk_add_f16 v166, v104, v145
	v_cvt_pk_f16_f32 v146, v48, v49
	v_cvt_pk_f16_f32 v147, v50, v51
	s_add_u32 s54, s88, 0xbd0000
	s_addc_u32 s55, s89, 0
	s_mov_b32 m0, s70
	s_nop 0
	global_load_lds_dwordx4 v165, s[54:55]
	s_add_u32 s54, s14, 0xbb8000
	s_addc_u32 s55, s15, 0
	s_cmp_lg_u32 0, -1
	s_cselect_b32 s53, 0, 0
	s_add_i32 s44, s53, s44
	s_add_i32 s53, s44, 0x14000
	s_mov_b32 m0, s53
	s_nop 0
	global_load_lds_dwordx4 v164, s[54:55]
	s_waitcnt lgkmcnt(14)
	v_mfma_f32_32x32x16_f16 v[4:19], v[124:127], v[148:151], v[4:19]
	v_exp_f32_e32 v84, v84
	v_exp_f32_e32 v85, v85
	v_exp_f32_e32 v86, v86
	v_exp_f32_e32 v87, v87
	s_waitcnt lgkmcnt(12)
	v_mfma_f32_32x32x16_f16 v[20:35], v[124:127], v[52:55], v[20:35]
	v_exp_f32_e32 v88, v88
	v_exp_f32_e32 v89, v89
	v_exp_f32_e32 v90, v90
	v_exp_f32_e32 v91, v91
	ds_read_b128 v[48:51], v210 offset:16384
	ds_read_b128 v[52:55], v210 offset:18432
	s_waitcnt lgkmcnt(12)
	v_mfma_f32_32x32x16_f16 v[4:19], v[120:123], v[56:59], v[4:19]
	v_exp_f32_e32 v92, v92
	v_exp_f32_e32 v93, v93
	v_exp_f32_e32 v94, v94
	v_exp_f32_e32 v95, v95
	ds_read_b128 v[56:59], v210 offset:16896
	ds_read_b128 v[148:151], v210 offset:18944
	s_waitcnt lgkmcnt(12)
	v_mfma_f32_32x32x16_f16 v[20:35], v[120:123], v[60:63], v[20:35]
	v_exp_f32_e32 v96, v96
	v_exp_f32_e32 v97, v97
	v_exp_f32_e32 v98, v98
	v_exp_f32_e32 v99, v99
	ds_read_b128 v[60:63], v210 offset:20480
	ds_read_b128 v[152:155], v210 offset:22528
	s_waitcnt lgkmcnt(12)
	v_mfma_f32_32x32x16_f16 v[4:19], v[116:119], v[64:67], v[4:19]
	v_exp_f32_e32 v68, v68
	v_exp_f32_e32 v69, v69
	v_exp_f32_e32 v70, v70
	v_exp_f32_e32 v71, v71
	ds_read_b128 v[64:67], v210 offset:20992
	ds_read_b128 v[156:159], v210 offset:23040
	s_waitcnt lgkmcnt(12)
	v_mfma_f32_32x32x16_f16 v[20:35], v[116:119], v[36:39], v[20:35]
	v_exp_f32_e32 v72, v72
	v_exp_f32_e32 v73, v73
	v_exp_f32_e32 v74, v74
	v_exp_f32_e32 v75, v75
	s_waitcnt lgkmcnt(10)
	v_mfma_f32_32x32x16_f16 v[4:19], v[144:147], v[40:43], v[4:19]
	v_exp_f32_e32 v76, v76
	v_exp_f32_e32 v77, v77
	v_exp_f32_e32 v78, v78
	v_exp_f32_e32 v79, v79
	s_waitcnt lgkmcnt(8)
	v_mfma_f32_32x32x16_f16 v[20:35], v[144:147], v[44:47], v[20:35]
	v_exp_f32_e32 v80, v80
	v_exp_f32_e32 v81, v81
	v_exp_f32_e32 v82, v82
	v_exp_f32_e32 v83, v83
	ds_read_b64_tr_b16 v[160:161], v211 offset:57344
	ds_read_b64_tr_b16 v[162:163], v211 offset:57856
	s_waitcnt lgkmcnt(9)
	v_mfma_f32_32x32x16_bf16 v[100:115], v[48:51], v[140:143], -4.0
	v_cvt_pk_f16_f32 v124, v84, v85
	v_pk_add_f16 v0, v0, v146
	v_pk_add_f16 v116, v166, v147
	v_cvt_pk_f16_f32 v125, v86, v87
	ds_read_b64_tr_b16 v[84:85], v211 offset:61440
	ds_read_b64_tr_b16 v[86:87], v211 offset:61952
	s_waitcnt lgkmcnt(10)
	v_mfma_f32_32x32x16_bf16 v[36:51], v[52:55], v[140:143], -4.0
	s_nop 0
	v_pk_add_f16 v0, v0, v124
	v_pk_add_f16 v116, v116, v125
	v_cvt_pk_f16_f32 v126, v88, v89
	v_cvt_pk_f16_f32 v127, v90, v91
	ds_read_b64_tr_b16 v[52:53], v211 offset:58368
	ds_read_b64_tr_b16 v[54:55], v211 offset:58880
	s_waitcnt lgkmcnt(11)
	v_mfma_f32_32x32x16_bf16 v[100:115], v[56:59], v[128:131], v[100:115]
	v_pk_add_f16 v0, v0, v126
	v_pk_add_f16 v88, v116, v127
	v_cvt_pk_f16_f32 v120, v92, v93
	v_cvt_pk_f16_f32 v121, v94, v95
	ds_read_b64_tr_b16 v[56:57], v211 offset:62464
	ds_read_b64_tr_b16 v[58:59], v211 offset:62976
	s_waitcnt lgkmcnt(12)
	v_mfma_f32_32x32x16_bf16 v[36:51], v[148:151], v[128:131], v[36:51]
	s_nop 0
	v_pk_add_f16 v0, v0, v120
	v_pk_add_f16 v92, v88, v121
	v_cvt_pk_f16_f32 v122, v96, v97
	v_cvt_pk_f16_f32 v123, v98, v99
	ds_read_b64_tr_b16 v[88:89], v211 offset:59392
	ds_read_b64_tr_b16 v[90:91], v211 offset:59904
	s_waitcnt lgkmcnt(13)
	v_mfma_f32_32x32x16_bf16 v[100:115], v[60:63], v[136:139], v[100:115]
	v_pk_add_f16 v0, v0, v122
	v_pk_add_f16 v92, v92, v123
	v_cvt_pk_f16_f32 v116, v68, v69
	v_cvt_pk_f16_f32 v117, v70, v71
	ds_read_b64_tr_b16 v[60:61], v211 offset:63488
	ds_read_b64_tr_b16 v[62:63], v211 offset:64000
	s_waitcnt lgkmcnt(14)
	v_mfma_f32_32x32x16_bf16 v[36:51], v[152:155], v[136:139], v[36:51]
	s_nop 0
	v_pk_add_f16 v0, v0, v116
	v_pk_add_f16 v68, v92, v117
	v_cvt_pk_f16_f32 v118, v72, v73
	v_cvt_pk_f16_f32 v119, v74, v75
	ds_read_b64_tr_b16 v[72:73], v211 offset:60416
	ds_read_b64_tr_b16 v[74:75], v211 offset:60928
	s_waitcnt lgkmcnt(14)
	v_mfma_f32_32x32x16_bf16 v[100:115], v[64:67], v[132:135], v[100:115]
	v_pk_add_f16 v0, v0, v118
	v_pk_add_f16 v68, v68, v119
	v_cvt_pk_f16_f32 v144, v76, v77
	v_cvt_pk_f16_f32 v145, v78, v79
	ds_read_b64_tr_b16 v[64:65], v211 offset:64512
	ds_read_b64_tr_b16 v[66:67], v211 offset:65024
	v_mfma_f32_32x32x16_bf16 v[36:51], v[156:159], v[132:135], v[36:51]
	s_nop 0
	v_pk_add_f16 v0, v0, v144
	v_pk_add_f16 v170, v68, v145
	v_cvt_pk_f16_f32 v146, v80, v81
	v_cvt_pk_f16_f32 v147, v82, v83
	s_add_u32 s54, s88, 0xbdc000
	s_addc_u32 s55, s89, 0
	s_add_i32 s53, s44, 0x2000
	s_mov_b32 m0, s53
	s_nop 0
	global_load_lds_dwordx4 v165, s[54:55]
	s_add_u32 s54, s14, 0xbc4000
	s_addc_u32 s55, s15, 0
	s_add_i32 s53, s44, 0x16000
	s_mov_b32 m0, s53
	s_nop 0
	global_load_lds_dwordx4 v164, s[54:55]
	s_waitcnt lgkmcnt(14)
	v_mfma_f32_32x32x16_f16 v[4:19], v[124:127], v[160:163], v[4:19]
	v_exp_f32_e32 v100, v100
	v_exp_f32_e32 v101, v101
	v_exp_f32_e32 v102, v102
	v_exp_f32_e32 v103, v103
	s_waitcnt lgkmcnt(12)
	v_mfma_f32_32x32x16_f16 v[20:35], v[124:127], v[84:87], v[20:35]
	v_exp_f32_e32 v104, v104
	v_exp_f32_e32 v105, v105
	v_exp_f32_e32 v106, v106
	v_exp_f32_e32 v107, v107
	ds_read_b128 v[76:79], v210 offset:24576
	ds_read_b128 v[80:83], v210 offset:26624
	s_waitcnt lgkmcnt(12)
	v_mfma_f32_32x32x16_f16 v[4:19], v[120:123], v[52:55], v[4:19]
	v_exp_f32_e32 v108, v108
	v_exp_f32_e32 v109, v109
	v_exp_f32_e32 v110, v110
	v_exp_f32_e32 v111, v111
	ds_read_b128 v[148:151], v210 offset:25088
	ds_read_b128 v[152:155], v210 offset:27136
	s_waitcnt lgkmcnt(12)
	v_mfma_f32_32x32x16_f16 v[20:35], v[120:123], v[56:59], v[20:35]
	v_exp_f32_e32 v112, v112
	v_exp_f32_e32 v113, v113
	v_exp_f32_e32 v114, v114
	v_exp_f32_e32 v115, v115
	ds_read_b128 v[156:159], v210 offset:28672
	ds_read_b128 v[160:163], v210 offset:30720
	s_waitcnt lgkmcnt(12)
	v_mfma_f32_32x32x16_f16 v[4:19], v[116:119], v[88:91], v[4:19]
	v_exp_f32_e32 v36, v36
	v_exp_f32_e32 v37, v37
	v_exp_f32_e32 v38, v38
	v_exp_f32_e32 v39, v39
	ds_read_b128 v[166:169], v210 offset:29184
	ds_read_b128 v[68:71], v210 offset:31232
	s_waitcnt lgkmcnt(12)
	v_mfma_f32_32x32x16_f16 v[20:35], v[116:119], v[60:63], v[20:35]
	v_exp_f32_e32 v40, v40
	v_exp_f32_e32 v41, v41
	v_exp_f32_e32 v42, v42
	v_exp_f32_e32 v43, v43
	s_waitcnt lgkmcnt(10)
	v_mfma_f32_32x32x16_f16 v[4:19], v[144:147], v[72:75], v[4:19]
	v_exp_f32_e32 v44, v44
	v_exp_f32_e32 v45, v45
	v_exp_f32_e32 v46, v46
	v_exp_f32_e32 v47, v47
	s_waitcnt lgkmcnt(8)
	v_mfma_f32_32x32x16_f16 v[20:35], v[144:147], v[64:67], v[20:35]
	v_exp_f32_e32 v48, v48
	v_exp_f32_e32 v49, v49
	v_exp_f32_e32 v50, v50
	v_exp_f32_e32 v51, v51
	s_waitcnt vmcnt(4) lgkmcnt(0)
	s_barrier
	ds_read_b64_tr_b16 v[72:73], v212 offset:16384
	ds_read_b64_tr_b16 v[74:75], v212 offset:16896
	s_waitcnt lgkmcnt(9)
	v_mfma_f32_32x32x16_bf16 v[84:99], v[76:79], v[140:143], -4.0
	v_cvt_pk_f16_f32 v124, v100, v101
	v_pk_add_f16 v0, v0, v146
	v_pk_add_f16 v52, v170, v147
	v_mov_b32_e32 v100, v3
	v_pk_add_f16 v0, v0, v52
	v_cvt_pk_f16_f32 v125, v102, v103
	v_dot2c_f32_f16_e32 v2, 0x3c003c00, v0
	v_mov_b32_e32 v0, v3
	ds_read_b64_tr_b16 v[76:77], v212 offset:20480
	ds_read_b64_tr_b16 v[78:79], v212 offset:20992
	s_waitcnt lgkmcnt(10)
	v_mfma_f32_32x32x16_bf16 v[52:67], v[80:83], v[140:143], -4.0
	s_nop 0
	v_pk_add_f16 v0, v0, v124
	v_pk_add_f16 v100, v100, v125
	v_cvt_pk_f16_f32 v126, v104, v105
	v_cvt_pk_f16_f32 v127, v106, v107
	ds_read_b64_tr_b16 v[80:81], v212 offset:17408
	ds_read_b64_tr_b16 v[82:83], v212 offset:17920
	s_waitcnt lgkmcnt(11)
	v_mfma_f32_32x32x16_bf16 v[84:99], v[148:151], v[128:131], v[84:99]
	v_pk_add_f16 v0, v0, v126
	v_pk_add_f16 v104, v100, v127
	v_cvt_pk_f16_f32 v120, v108, v109
	v_cvt_pk_f16_f32 v121, v110, v111
	ds_read_b64_tr_b16 v[100:101], v212 offset:21504
	ds_read_b64_tr_b16 v[102:103], v212 offset:22016
	s_waitcnt lgkmcnt(12)
	v_mfma_f32_32x32x16_bf16 v[52:67], v[152:155], v[128:131], v[52:67]
	v_pk_add_f16 v0, v0, v120
	v_pk_add_f16 v108, v104, v121
	v_cvt_pk_f16_f32 v122, v112, v113
	v_cvt_pk_f16_f32 v123, v114, v115
	ds_read_b64_tr_b16 v[104:105], v212 offset:18432
	ds_read_b64_tr_b16 v[106:107], v212 offset:18944
	s_waitcnt lgkmcnt(13)
	v_mfma_f32_32x32x16_bf16 v[84:99], v[156:159], v[136:139], v[84:99]
	v_pk_add_f16 v0, v0, v122
	v_pk_add_f16 v108, v108, v123
	v_cvt_pk_f16_f32 v116, v36, v37
	v_cvt_pk_f16_f32 v117, v38, v39
	ds_read_b64_tr_b16 v[36:37], v212 offset:22528
	ds_read_b64_tr_b16 v[38:39], v212 offset:23040
	s_waitcnt lgkmcnt(14)
	v_mfma_f32_32x32x16_bf16 v[52:67], v[160:163], v[136:139], v[52:67]
	v_pk_add_f16 v0, v0, v116
	v_pk_add_f16 v108, v108, v117
	v_cvt_pk_f16_f32 v118, v40, v41
	v_cvt_pk_f16_f32 v119, v42, v43
	ds_read_b64_tr_b16 v[40:41], v212 offset:19456
	ds_read_b64_tr_b16 v[42:43], v212 offset:19968
	s_waitcnt lgkmcnt(14)
	v_mfma_f32_32x32x16_bf16 v[84:99], v[166:169], v[132:135], v[84:99]
	v_pk_add_f16 v0, v0, v118
	v_pk_add_f16 v108, v108, v119
	v_cvt_pk_f16_f32 v144, v44, v45
	v_cvt_pk_f16_f32 v145, v46, v47
	ds_read_b64_tr_b16 v[44:45], v212 offset:23552
	ds_read_b64_tr_b16 v[46:47], v212 offset:24064
	v_mfma_f32_32x32x16_bf16 v[52:67], v[68:71], v[132:135], v[52:67]
	v_pk_add_f16 v0, v0, v144
	v_pk_add_f16 v166, v108, v145
	v_cvt_pk_f16_f32 v146, v48, v49
	v_cvt_pk_f16_f32 v147, v50, v51
	s_add_u32 s54, s88, 0xbe8000
	s_addc_u32 s55, s89, 0
	s_add_i32 s53, s44, 0x4000
	s_mov_b32 m0, s53
	s_nop 0
	global_load_lds_dwordx4 v165, s[54:55]
	s_add_u32 s54, s14, 0xbd0000
	s_addc_u32 s55, s15, 0
	s_mov_b32 m0, s10
	s_nop 0
	global_load_lds_dwordx4 v164, s[54:55]
	s_waitcnt lgkmcnt(14)
	v_mfma_f32_32x32x16_f16 v[4:19], v[124:127], v[72:75], v[4:19]
	v_exp_f32_e32 v84, v84
	v_exp_f32_e32 v85, v85
	v_exp_f32_e32 v86, v86
	v_exp_f32_e32 v87, v87
	s_waitcnt lgkmcnt(12)
	v_mfma_f32_32x32x16_f16 v[20:35], v[124:127], v[76:79], v[20:35]
	v_exp_f32_e32 v88, v88
	v_exp_f32_e32 v89, v89
	v_exp_f32_e32 v90, v90
	v_exp_f32_e32 v91, v91
	ds_read_b128 v[48:51], v210 offset:32768
	ds_read_b128 v[108:111], v210 offset:34816
	s_waitcnt lgkmcnt(12)
	v_mfma_f32_32x32x16_f16 v[4:19], v[120:123], v[80:83], v[4:19]
	v_exp_f32_e32 v92, v92
	v_exp_f32_e32 v93, v93
	v_exp_f32_e32 v94, v94
	v_exp_f32_e32 v95, v95
	ds_read_b128 v[112:115], v210 offset:33280
	ds_read_b128 v[148:151], v210 offset:35328
	s_waitcnt lgkmcnt(12)
	v_mfma_f32_32x32x16_f16 v[20:35], v[120:123], v[100:103], v[20:35]
	v_exp_f32_e32 v96, v96
	v_exp_f32_e32 v97, v97
	v_exp_f32_e32 v98, v98
	v_exp_f32_e32 v99, v99
	ds_read_b128 v[100:103], v210 offset:36864
	ds_read_b128 v[152:155], v210 offset:38912
	s_waitcnt lgkmcnt(12)
	v_mfma_f32_32x32x16_f16 v[4:19], v[116:119], v[104:107], v[4:19]
	v_exp_f32_e32 v52, v52
	v_exp_f32_e32 v53, v53
	v_exp_f32_e32 v54, v54
	v_exp_f32_e32 v55, v55
	ds_read_b128 v[104:107], v210 offset:37376
	ds_read_b128 v[156:159], v210 offset:39424
	s_waitcnt lgkmcnt(12)
	v_mfma_f32_32x32x16_f16 v[20:35], v[116:119], v[36:39], v[20:35]
	v_exp_f32_e32 v56, v56
	v_exp_f32_e32 v57, v57
	v_exp_f32_e32 v58, v58
	v_exp_f32_e32 v59, v59
	s_waitcnt lgkmcnt(10)
	v_mfma_f32_32x32x16_f16 v[4:19], v[144:147], v[40:43], v[4:19]
	v_exp_f32_e32 v60, v60
	v_exp_f32_e32 v61, v61
	v_exp_f32_e32 v62, v62
	v_exp_f32_e32 v63, v63
	s_waitcnt lgkmcnt(8)
	v_mfma_f32_32x32x16_f16 v[20:35], v[144:147], v[44:47], v[20:35]
	v_exp_f32_e32 v64, v64
	v_exp_f32_e32 v65, v65
	v_exp_f32_e32 v66, v66
	v_exp_f32_e32 v67, v67
	ds_read_b64_tr_b16 v[160:161], v212 offset:24576
	ds_read_b64_tr_b16 v[162:163], v212 offset:25088
	s_waitcnt lgkmcnt(9)
	v_mfma_f32_32x32x16_bf16 v[68:83], v[48:51], v[140:143], -4.0
	v_cvt_pk_f16_f32 v124, v84, v85
	v_pk_add_f16 v0, v0, v146
	v_pk_add_f16 v116, v166, v147
	v_cvt_pk_f16_f32 v125, v86, v87
	ds_read_b64_tr_b16 v[84:85], v212 offset:28672
	ds_read_b64_tr_b16 v[86:87], v212 offset:29184
	s_waitcnt lgkmcnt(10)
	v_mfma_f32_32x32x16_bf16 v[36:51], v[108:111], v[140:143], -4.0
	s_nop 0
	v_pk_add_f16 v0, v0, v124
	v_pk_add_f16 v108, v116, v125
	v_cvt_pk_f16_f32 v126, v88, v89
	v_cvt_pk_f16_f32 v127, v90, v91
	ds_read_b64_tr_b16 v[88:89], v212 offset:25600
	ds_read_b64_tr_b16 v[90:91], v212 offset:26112
	s_waitcnt lgkmcnt(11)
	v_mfma_f32_32x32x16_bf16 v[68:83], v[112:115], v[128:131], v[68:83]
	v_pk_add_f16 v0, v0, v126
	v_pk_add_f16 v108, v108, v127
	v_cvt_pk_f16_f32 v120, v92, v93
	v_cvt_pk_f16_f32 v121, v94, v95
	ds_read_b64_tr_b16 v[92:93], v212 offset:29696
	ds_read_b64_tr_b16 v[94:95], v212 offset:30208
	s_waitcnt lgkmcnt(12)
	v_mfma_f32_32x32x16_bf16 v[36:51], v[148:151], v[128:131], v[36:51]
	s_nop 0
	v_pk_add_f16 v0, v0, v120
	v_pk_add_f16 v108, v108, v121
	v_cvt_pk_f16_f32 v122, v96, v97
	v_cvt_pk_f16_f32 v123, v98, v99
	ds_read_b64_tr_b16 v[96:97], v212 offset:26624
	ds_read_b64_tr_b16 v[98:99], v212 offset:27136
	s_waitcnt lgkmcnt(13)
	v_mfma_f32_32x32x16_bf16 v[68:83], v[100:103], v[136:139], v[68:83]
	v_cvt_pk_f16_f32 v116, v52, v53
	v_pk_add_f16 v0, v0, v122
	v_pk_add_f16 v100, v108, v123
	v_cvt_pk_f16_f32 v117, v54, v55
	ds_read_b64_tr_b16 v[52:53], v212 offset:30720
	ds_read_b64_tr_b16 v[54:55], v212 offset:31232
	s_waitcnt lgkmcnt(14)
	v_mfma_f32_32x32x16_bf16 v[36:51], v[152:155], v[136:139], v[36:51]
	s_nop 0
	v_pk_add_f16 v0, v0, v116
	v_pk_add_f16 v100, v100, v117
	v_cvt_pk_f16_f32 v118, v56, v57
	v_cvt_pk_f16_f32 v119, v58, v59
	ds_read_b64_tr_b16 v[56:57], v212 offset:27648
	ds_read_b64_tr_b16 v[58:59], v212 offset:28160
	s_waitcnt lgkmcnt(14)
	v_mfma_f32_32x32x16_bf16 v[68:83], v[104:107], v[132:135], v[68:83]
	v_pk_add_f16 v0, v0, v118
	v_pk_add_f16 v100, v100, v119
	v_cvt_pk_f16_f32 v144, v60, v61
	v_cvt_pk_f16_f32 v145, v62, v63
	ds_read_b64_tr_b16 v[60:61], v212 offset:31744
	ds_read_b64_tr_b16 v[62:63], v212 offset:32256
	v_mfma_f32_32x32x16_bf16 v[36:51], v[156:159], v[132:135], v[36:51]
	s_nop 0
	v_pk_add_f16 v0, v0, v144
	v_pk_add_f16 v166, v100, v145
	v_cvt_pk_f16_f32 v146, v64, v65
	v_cvt_pk_f16_f32 v147, v66, v67
	s_add_u32 s54, s88, 0xbf4000
	s_addc_u32 s55, s89, 0
	s_add_i32 s10, s44, 0x6000
	s_mov_b32 m0, s10
	s_nop 0
	global_load_lds_dwordx4 v165, s[54:55]
	s_add_u32 s54, s14, 0xbdc000
	s_addc_u32 s55, s15, 0
	s_add_i32 s10, s44, 0xe000
	s_mov_b32 m0, s10
	s_nop 0
	global_load_lds_dwordx4 v164, s[54:55]
	s_waitcnt lgkmcnt(14)
	v_mfma_f32_32x32x16_f16 v[4:19], v[124:127], v[160:163], v[4:19]
	v_exp_f32_e32 v68, v68
	v_exp_f32_e32 v69, v69
	v_exp_f32_e32 v70, v70
	v_exp_f32_e32 v71, v71
	s_waitcnt lgkmcnt(12)
	v_mfma_f32_32x32x16_f16 v[20:35], v[124:127], v[84:87], v[20:35]
	v_exp_f32_e32 v72, v72
	v_exp_f32_e32 v73, v73
	v_exp_f32_e32 v74, v74
	v_exp_f32_e32 v75, v75
	ds_read_b128 v[64:67], v210 offset:40960
	ds_read_b128 v[104:107], v210 offset:43008
	s_waitcnt lgkmcnt(12)
	v_mfma_f32_32x32x16_f16 v[4:19], v[120:123], v[88:91], v[4:19]
	v_exp_f32_e32 v76, v76
	v_exp_f32_e32 v77, v77
	v_exp_f32_e32 v78, v78
	v_exp_f32_e32 v79, v79
	ds_read_b128 v[108:111], v210 offset:41472
	ds_read_b128 v[112:115], v210 offset:43520
	s_waitcnt lgkmcnt(12)
	v_mfma_f32_32x32x16_f16 v[20:35], v[120:123], v[92:95], v[20:35]
	v_exp_f32_e32 v80, v80
	v_exp_f32_e32 v81, v81
	v_exp_f32_e32 v82, v82
	v_exp_f32_e32 v83, v83
	ds_read_b128 v[148:151], v210 offset:45056
	ds_read_b128 v[152:155], v210 offset:47104
	s_waitcnt lgkmcnt(12)
	v_mfma_f32_32x32x16_f16 v[4:19], v[116:119], v[96:99], v[4:19]
	v_exp_f32_e32 v36, v36
	v_exp_f32_e32 v37, v37
	v_exp_f32_e32 v38, v38
	v_exp_f32_e32 v39, v39
	ds_read_b128 v[156:159], v210 offset:45568
	ds_read_b128 v[100:103], v210 offset:47616
	s_waitcnt lgkmcnt(12)
	v_mfma_f32_32x32x16_f16 v[20:35], v[116:119], v[52:55], v[20:35]
	v_exp_f32_e32 v40, v40
	v_exp_f32_e32 v41, v41
	v_exp_f32_e32 v42, v42
	v_exp_f32_e32 v43, v43
	s_waitcnt lgkmcnt(10)
	v_mfma_f32_32x32x16_f16 v[4:19], v[144:147], v[56:59], v[4:19]
	v_exp_f32_e32 v44, v44
	v_exp_f32_e32 v45, v45
	v_exp_f32_e32 v46, v46
	v_exp_f32_e32 v47, v47
	s_waitcnt lgkmcnt(8)
	v_mfma_f32_32x32x16_f16 v[20:35], v[144:147], v[60:63], v[20:35]
	v_exp_f32_e32 v48, v48
	v_exp_f32_e32 v49, v49
	v_exp_f32_e32 v50, v50
	v_exp_f32_e32 v51, v51
	s_waitcnt vmcnt(4) lgkmcnt(0)
	s_barrier
	ds_read_b64_tr_b16 v[160:161], v212 offset:32768
	ds_read_b64_tr_b16 v[162:163], v212 offset:33280
	s_waitcnt lgkmcnt(9)
	v_mfma_f32_32x32x16_bf16 v[84:99], v[64:67], v[140:143], -4.0
	v_mov_b32_e32 v116, v3
	v_pk_add_f16 v0, v0, v146
	v_pk_add_f16 v52, v166, v147
	v_cvt_pk_f16_f32 v124, v68, v69
	v_pk_add_f16 v0, v0, v52
	v_cvt_pk_f16_f32 v125, v70, v71
	v_dot2c_f32_f16_e32 v2, 0x3c003c00, v0
	v_mov_b32_e32 v0, v3
	ds_read_b64_tr_b16 v[68:69], v212 offset:36864
	ds_read_b64_tr_b16 v[70:71], v212 offset:37376
	s_waitcnt lgkmcnt(10)
	v_mfma_f32_32x32x16_bf16 v[52:67], v[104:107], v[140:143], -4.0
	s_nop 0
	v_pk_add_f16 v0, v0, v124
	v_pk_add_f16 v104, v116, v125
	v_cvt_pk_f16_f32 v126, v72, v73
	v_cvt_pk_f16_f32 v127, v74, v75
	ds_read_b64_tr_b16 v[72:73], v212 offset:33792
	ds_read_b64_tr_b16 v[74:75], v212 offset:34304
	s_waitcnt lgkmcnt(11)
	v_mfma_f32_32x32x16_bf16 v[84:99], v[108:111], v[128:131], v[84:99]
	v_pk_add_f16 v0, v0, v126
	v_pk_add_f16 v104, v104, v127
	v_cvt_pk_f16_f32 v120, v76, v77
	v_cvt_pk_f16_f32 v121, v78, v79
	ds_read_b64_tr_b16 v[76:77], v212 offset:37888
	ds_read_b64_tr_b16 v[78:79], v212 offset:38400
	s_waitcnt lgkmcnt(12)
	v_mfma_f32_32x32x16_bf16 v[52:67], v[112:115], v[128:131], v[52:67]
	v_pk_add_f16 v0, v0, v120
	v_pk_add_f16 v104, v104, v121
	v_cvt_pk_f16_f32 v122, v80, v81
	v_cvt_pk_f16_f32 v123, v82, v83
	ds_read_b64_tr_b16 v[80:81], v212 offset:34816
	ds_read_b64_tr_b16 v[82:83], v212 offset:35328
	s_waitcnt lgkmcnt(13)
	v_mfma_f32_32x32x16_bf16 v[84:99], v[148:151], v[136:139], v[84:99]
	v_pk_add_f16 v0, v0, v122
	v_pk_add_f16 v104, v104, v123
	v_cvt_pk_f16_f32 v116, v36, v37
	v_cvt_pk_f16_f32 v117, v38, v39
	ds_read_b64_tr_b16 v[36:37], v212 offset:38912
	ds_read_b64_tr_b16 v[38:39], v212 offset:39424
	s_waitcnt lgkmcnt(14)
	v_mfma_f32_32x32x16_bf16 v[52:67], v[152:155], v[136:139], v[52:67]
	v_pk_add_f16 v0, v0, v116
	v_pk_add_f16 v104, v104, v117
	v_cvt_pk_f16_f32 v118, v40, v41
	v_cvt_pk_f16_f32 v119, v42, v43
	ds_read_b64_tr_b16 v[40:41], v212 offset:35840
	ds_read_b64_tr_b16 v[42:43], v212 offset:36352
	s_waitcnt lgkmcnt(14)
	v_mfma_f32_32x32x16_bf16 v[84:99], v[156:159], v[132:135], v[84:99]
	v_pk_add_f16 v0, v0, v118
	v_pk_add_f16 v104, v104, v119
	v_cvt_pk_f16_f32 v144, v44, v45
	v_cvt_pk_f16_f32 v145, v46, v47
	ds_read_b64_tr_b16 v[44:45], v212 offset:39936
	ds_read_b64_tr_b16 v[46:47], v212 offset:40448
	v_mfma_f32_32x32x16_bf16 v[52:67], v[100:103], v[132:135], v[52:67]
	v_pk_add_f16 v0, v0, v144
	v_pk_add_f16 v165, v104, v145
	v_cvt_pk_f16_f32 v146, v48, v49
	v_cvt_pk_f16_f32 v147, v50, v51
	s_add_u32 s54, s14, 0xbe8000
	s_addc_u32 s55, s15, 0
	s_add_i32 s10, s44, 0x10000
	s_mov_b32 m0, s10
	s_nop 0
	global_load_lds_dwordx4 v164, s[54:55]
	s_waitcnt lgkmcnt(14)
	v_mfma_f32_32x32x16_f16 v[4:19], v[124:127], v[160:163], v[4:19]
	v_exp_f32_e32 v84, v84
	v_exp_f32_e32 v85, v85
	v_exp_f32_e32 v86, v86
	v_exp_f32_e32 v87, v87
	s_waitcnt lgkmcnt(12)
	v_mfma_f32_32x32x16_f16 v[20:35], v[124:127], v[68:71], v[20:35]
	v_exp_f32_e32 v88, v88
	v_exp_f32_e32 v89, v89
	v_exp_f32_e32 v90, v90
	v_exp_f32_e32 v91, v91
	ds_read_b128 v[48:51], v210
	ds_read_b128 v[100:103], v210 offset:2048
	s_waitcnt lgkmcnt(12)
	v_mfma_f32_32x32x16_f16 v[4:19], v[120:123], v[72:75], v[4:19]
	v_exp_f32_e32 v92, v92
	v_exp_f32_e32 v93, v93
	v_exp_f32_e32 v94, v94
	v_exp_f32_e32 v95, v95
	ds_read_b128 v[104:107], v210 offset:512
	ds_read_b128 v[108:111], v210 offset:2560
	s_waitcnt lgkmcnt(12)
	v_mfma_f32_32x32x16_f16 v[20:35], v[120:123], v[76:79], v[20:35]
	v_exp_f32_e32 v96, v96
	v_exp_f32_e32 v97, v97
	v_exp_f32_e32 v98, v98
	v_exp_f32_e32 v99, v99
	ds_read_b128 v[112:115], v210 offset:4096
	ds_read_b128 v[148:151], v210 offset:6144
	s_waitcnt lgkmcnt(12)
	v_mfma_f32_32x32x16_f16 v[4:19], v[116:119], v[80:83], v[4:19]
	v_exp_f32_e32 v52, v52
	v_exp_f32_e32 v53, v53
	v_exp_f32_e32 v54, v54
	v_exp_f32_e32 v55, v55
	ds_read_b128 v[152:155], v210 offset:4608
	ds_read_b128 v[156:159], v210 offset:6656
	s_waitcnt lgkmcnt(12)
	v_mfma_f32_32x32x16_f16 v[20:35], v[116:119], v[36:39], v[20:35]
	v_exp_f32_e32 v56, v56
	v_exp_f32_e32 v57, v57
	v_exp_f32_e32 v58, v58
	v_exp_f32_e32 v59, v59
	s_waitcnt lgkmcnt(10)
	v_mfma_f32_32x32x16_f16 v[4:19], v[144:147], v[40:43], v[4:19]
	v_exp_f32_e32 v60, v60
	v_exp_f32_e32 v61, v61
	v_exp_f32_e32 v62, v62
	v_exp_f32_e32 v63, v63
	s_waitcnt lgkmcnt(8)
	v_mfma_f32_32x32x16_f16 v[20:35], v[144:147], v[44:47], v[20:35]
	v_exp_f32_e32 v64, v64
	v_exp_f32_e32 v65, v65
	v_exp_f32_e32 v66, v66
	v_exp_f32_e32 v67, v67
	ds_read_b64_tr_b16 v[160:161], v212 offset:40960
	ds_read_b64_tr_b16 v[162:163], v212 offset:41472
	s_waitcnt lgkmcnt(9)
	v_mfma_f32_32x32x16_bf16 v[68:83], v[48:51], v[140:143], -4.0
	v_cvt_pk_f16_f32 v124, v84, v85
	v_pk_add_f16 v0, v0, v146
	v_pk_add_f16 v116, v165, v147
	v_cvt_pk_f16_f32 v125, v86, v87
	ds_read_b64_tr_b16 v[84:85], v212 offset:45056
	ds_read_b64_tr_b16 v[86:87], v212 offset:45568
	s_waitcnt lgkmcnt(10)
	v_mfma_f32_32x32x16_bf16 v[36:51], v[100:103], v[140:143], -4.0
	s_nop 0
	v_pk_add_f16 v0, v0, v124
	v_pk_add_f16 v100, v116, v125
	v_cvt_pk_f16_f32 v126, v88, v89
	v_cvt_pk_f16_f32 v127, v90, v91
	ds_read_b64_tr_b16 v[88:89], v212 offset:41984
	ds_read_b64_tr_b16 v[90:91], v212 offset:42496
	s_waitcnt lgkmcnt(11)
	v_mfma_f32_32x32x16_bf16 v[68:83], v[104:107], v[128:131], v[68:83]
	v_pk_add_f16 v0, v0, v126
	v_pk_add_f16 v100, v100, v127
	v_cvt_pk_f16_f32 v120, v92, v93
	v_cvt_pk_f16_f32 v121, v94, v95
	ds_read_b64_tr_b16 v[92:93], v212 offset:46080
	ds_read_b64_tr_b16 v[94:95], v212 offset:46592
	s_waitcnt lgkmcnt(12)
	v_mfma_f32_32x32x16_bf16 v[36:51], v[108:111], v[128:131], v[36:51]
	s_nop 0
	v_pk_add_f16 v0, v0, v120
	v_pk_add_f16 v100, v100, v121
	v_cvt_pk_f16_f32 v122, v96, v97
	v_cvt_pk_f16_f32 v123, v98, v99
	ds_read_b64_tr_b16 v[96:97], v212 offset:43008
	ds_read_b64_tr_b16 v[98:99], v212 offset:43520
	s_waitcnt lgkmcnt(13)
	v_mfma_f32_32x32x16_bf16 v[68:83], v[112:115], v[136:139], v[68:83]
	v_pk_add_f16 v0, v0, v122
	v_pk_add_f16 v100, v100, v123
	v_cvt_pk_f16_f32 v116, v52, v53
	v_cvt_pk_f16_f32 v117, v54, v55
	ds_read_b64_tr_b16 v[52:53], v212 offset:47104
	ds_read_b64_tr_b16 v[54:55], v212 offset:47616
	s_waitcnt lgkmcnt(14)
	v_mfma_f32_32x32x16_bf16 v[36:51], v[148:151], v[136:139], v[36:51]
	s_nop 0
	v_pk_add_f16 v0, v0, v116
	v_pk_add_f16 v100, v100, v117
	v_cvt_pk_f16_f32 v118, v56, v57
	v_cvt_pk_f16_f32 v119, v58, v59
	ds_read_b64_tr_b16 v[56:57], v212 offset:44032
	ds_read_b64_tr_b16 v[58:59], v212 offset:44544
	s_waitcnt lgkmcnt(14)
	v_mfma_f32_32x32x16_bf16 v[68:83], v[152:155], v[132:135], v[68:83]
	v_pk_add_f16 v0, v0, v118
	v_pk_add_f16 v100, v100, v119
	v_cvt_pk_f16_f32 v144, v60, v61
	v_cvt_pk_f16_f32 v145, v62, v63
	ds_read_b64_tr_b16 v[60:61], v212 offset:48128
	ds_read_b64_tr_b16 v[62:63], v212 offset:48640
	v_mfma_f32_32x32x16_bf16 v[36:51], v[156:159], v[132:135], v[36:51]
	s_nop 0
	v_pk_add_f16 v0, v0, v144
	v_pk_add_f16 v165, v100, v145
	v_cvt_pk_f16_f32 v146, v64, v65
	v_cvt_pk_f16_f32 v147, v66, v67
	s_add_u32 s14, s14, 0xbf4000
	s_addc_u32 s15, s15, 0
	s_add_i32 s44, s44, 0x12000
	s_mov_b32 m0, s44
	s_nop 0
	global_load_lds_dwordx4 v164, s[14:15]
	s_waitcnt lgkmcnt(14)
	v_mfma_f32_32x32x16_f16 v[4:19], v[124:127], v[160:163], v[4:19]
	v_exp_f32_e32 v68, v68
	v_exp_f32_e32 v69, v69
	v_exp_f32_e32 v70, v70
	v_exp_f32_e32 v71, v71
	s_waitcnt lgkmcnt(12)
	v_mfma_f32_32x32x16_f16 v[20:35], v[124:127], v[84:87], v[20:35]
	v_exp_f32_e32 v72, v72
	v_exp_f32_e32 v73, v73
	v_exp_f32_e32 v74, v74
	v_exp_f32_e32 v75, v75
	ds_read_b128 v[64:67], v210 offset:8192
	ds_read_b128 v[104:107], v210 offset:10240
	s_waitcnt lgkmcnt(12)
	v_mfma_f32_32x32x16_f16 v[4:19], v[120:123], v[88:91], v[4:19]
	v_exp_f32_e32 v76, v76
	v_exp_f32_e32 v77, v77
	v_exp_f32_e32 v78, v78
	v_exp_f32_e32 v79, v79
	ds_read_b128 v[108:111], v210 offset:8704
	ds_read_b128 v[112:115], v210 offset:10752
	s_waitcnt lgkmcnt(12)
	v_mfma_f32_32x32x16_f16 v[20:35], v[120:123], v[92:95], v[20:35]
	v_exp_f32_e32 v80, v80
	v_exp_f32_e32 v81, v81
	v_exp_f32_e32 v82, v82
	v_exp_f32_e32 v83, v83
	ds_read_b128 v[148:151], v210 offset:12288
	ds_read_b128 v[152:155], v210 offset:14336
	s_waitcnt lgkmcnt(12)
	v_mfma_f32_32x32x16_f16 v[4:19], v[116:119], v[96:99], v[4:19]
	v_exp_f32_e32 v36, v36
	v_exp_f32_e32 v37, v37
	v_exp_f32_e32 v38, v38
	v_exp_f32_e32 v39, v39
	ds_read_b128 v[156:159], v210 offset:12800
	ds_read_b128 v[100:103], v210 offset:14848
	s_waitcnt lgkmcnt(12)
	v_mfma_f32_32x32x16_f16 v[20:35], v[116:119], v[52:55], v[20:35]
	v_exp_f32_e32 v40, v40
	v_exp_f32_e32 v41, v41
	v_exp_f32_e32 v42, v42
	v_exp_f32_e32 v43, v43
	s_waitcnt lgkmcnt(10)
	v_mfma_f32_32x32x16_f16 v[4:19], v[144:147], v[56:59], v[4:19]
	v_exp_f32_e32 v44, v44
	v_exp_f32_e32 v45, v45
	v_exp_f32_e32 v46, v46
	v_exp_f32_e32 v47, v47
	s_waitcnt lgkmcnt(8)
	v_mfma_f32_32x32x16_f16 v[20:35], v[144:147], v[60:63], v[20:35]
	v_exp_f32_e32 v48, v48
	v_exp_f32_e32 v49, v49
	v_exp_f32_e32 v50, v50
	v_exp_f32_e32 v51, v51
	s_waitcnt vmcnt(2) lgkmcnt(0)
	s_barrier
	ds_read_b64_tr_b16 v[160:161], v211 offset:49152
	ds_read_b64_tr_b16 v[162:163], v211 offset:49664
	s_waitcnt lgkmcnt(9)
	v_mfma_f32_32x32x16_bf16 v[84:99], v[64:67], v[140:143], -4.0
	v_mov_b32_e32 v116, v3
	v_pk_add_f16 v0, v0, v146
	v_pk_add_f16 v52, v165, v147
	v_cvt_pk_f16_f32 v124, v68, v69
	v_pk_add_f16 v0, v0, v52
	v_cvt_pk_f16_f32 v125, v70, v71
	v_dot2c_f32_f16_e32 v2, 0x3c003c00, v0
	v_mov_b32_e32 v0, v3
	ds_read_b64_tr_b16 v[68:69], v211 offset:53248
	ds_read_b64_tr_b16 v[70:71], v211 offset:53760
	s_waitcnt lgkmcnt(10)
	v_mfma_f32_32x32x16_bf16 v[52:67], v[104:107], v[140:143], -4.0
	s_nop 0
	v_pk_add_f16 v0, v0, v124
	v_pk_add_f16 v104, v116, v125
	v_cvt_pk_f16_f32 v126, v72, v73
	v_cvt_pk_f16_f32 v127, v74, v75
	ds_read_b64_tr_b16 v[72:73], v211 offset:50176
	ds_read_b64_tr_b16 v[74:75], v211 offset:50688
	s_waitcnt lgkmcnt(11)
	v_mfma_f32_32x32x16_bf16 v[84:99], v[108:111], v[128:131], v[84:99]
	v_pk_add_f16 v0, v0, v126
	v_pk_add_f16 v104, v104, v127
	v_cvt_pk_f16_f32 v120, v76, v77
	v_cvt_pk_f16_f32 v121, v78, v79
	ds_read_b64_tr_b16 v[76:77], v211 offset:54272
	ds_read_b64_tr_b16 v[78:79], v211 offset:54784
	s_waitcnt lgkmcnt(12)
	v_mfma_f32_32x32x16_bf16 v[52:67], v[112:115], v[128:131], v[52:67]
	v_pk_add_f16 v0, v0, v120
	v_pk_add_f16 v104, v104, v121
	v_cvt_pk_f16_f32 v122, v80, v81
	v_cvt_pk_f16_f32 v123, v82, v83
	ds_read_b64_tr_b16 v[80:81], v211 offset:51200
	ds_read_b64_tr_b16 v[82:83], v211 offset:51712
	s_waitcnt lgkmcnt(13)
	v_mfma_f32_32x32x16_bf16 v[84:99], v[148:151], v[136:139], v[84:99]
	v_pk_add_f16 v0, v0, v122
	v_pk_add_f16 v104, v104, v123
	v_cvt_pk_f16_f32 v116, v36, v37
	v_cvt_pk_f16_f32 v117, v38, v39
	ds_read_b64_tr_b16 v[36:37], v211 offset:55296
	ds_read_b64_tr_b16 v[38:39], v211 offset:55808
	s_waitcnt lgkmcnt(14)
	v_mfma_f32_32x32x16_bf16 v[52:67], v[152:155], v[136:139], v[52:67]
	v_pk_add_f16 v0, v0, v116
	v_pk_add_f16 v104, v104, v117
	v_cvt_pk_f16_f32 v118, v40, v41
	v_cvt_pk_f16_f32 v119, v42, v43
	ds_read_b64_tr_b16 v[40:41], v211 offset:52224
	ds_read_b64_tr_b16 v[42:43], v211 offset:52736
	s_waitcnt lgkmcnt(14)
	v_mfma_f32_32x32x16_bf16 v[84:99], v[156:159], v[132:135], v[84:99]
	v_pk_add_f16 v0, v0, v118
	v_pk_add_f16 v104, v104, v119
	v_cvt_pk_f16_f32 v144, v44, v45
	v_cvt_pk_f16_f32 v145, v46, v47
	ds_read_b64_tr_b16 v[44:45], v211 offset:56320
	ds_read_b64_tr_b16 v[46:47], v211 offset:56832
	v_mfma_f32_32x32x16_bf16 v[52:67], v[100:103], v[132:135], v[52:67]
	v_pk_add_f16 v0, v0, v144
	v_pk_add_f16 v164, v104, v145
	v_cvt_pk_f16_f32 v146, v48, v49
	v_cvt_pk_f16_f32 v147, v50, v51
	s_waitcnt lgkmcnt(14)
	v_mfma_f32_32x32x16_f16 v[4:19], v[124:127], v[160:163], v[4:19]
	v_exp_f32_e32 v84, v84
	v_exp_f32_e32 v85, v85
	v_exp_f32_e32 v86, v86
	v_exp_f32_e32 v87, v87
	s_waitcnt lgkmcnt(12)
	v_mfma_f32_32x32x16_f16 v[20:35], v[124:127], v[68:71], v[20:35]
	v_exp_f32_e32 v88, v88
	v_exp_f32_e32 v89, v89
	v_exp_f32_e32 v90, v90
	v_exp_f32_e32 v91, v91
	ds_read_b128 v[48:51], v210 offset:16384
	ds_read_b128 v[100:103], v210 offset:18432
	s_waitcnt lgkmcnt(12)
	v_mfma_f32_32x32x16_f16 v[4:19], v[120:123], v[72:75], v[4:19]
	v_exp_f32_e32 v92, v92
	v_exp_f32_e32 v93, v93
	v_exp_f32_e32 v94, v94
	v_exp_f32_e32 v95, v95
	ds_read_b128 v[104:107], v210 offset:16896
	ds_read_b128 v[108:111], v210 offset:18944
	s_waitcnt lgkmcnt(12)
	v_mfma_f32_32x32x16_f16 v[20:35], v[120:123], v[76:79], v[20:35]
	v_exp_f32_e32 v96, v96
	v_exp_f32_e32 v97, v97
	v_exp_f32_e32 v98, v98
	v_exp_f32_e32 v99, v99
	ds_read_b128 v[112:115], v210 offset:20480
	ds_read_b128 v[148:151], v210 offset:22528
	s_waitcnt lgkmcnt(12)
	v_mfma_f32_32x32x16_f16 v[4:19], v[116:119], v[80:83], v[4:19]
	v_exp_f32_e32 v52, v52
	v_exp_f32_e32 v53, v53
	v_exp_f32_e32 v54, v54
	v_exp_f32_e32 v55, v55
	ds_read_b128 v[152:155], v210 offset:20992
	ds_read_b128 v[156:159], v210 offset:23040
	s_waitcnt lgkmcnt(12)
	v_mfma_f32_32x32x16_f16 v[20:35], v[116:119], v[36:39], v[20:35]
	v_exp_f32_e32 v56, v56
	v_exp_f32_e32 v57, v57
	v_exp_f32_e32 v58, v58
	v_exp_f32_e32 v59, v59
	s_waitcnt lgkmcnt(10)
	v_mfma_f32_32x32x16_f16 v[4:19], v[144:147], v[40:43], v[4:19]
	v_exp_f32_e32 v60, v60
	v_exp_f32_e32 v61, v61
	v_exp_f32_e32 v62, v62
	v_exp_f32_e32 v63, v63
	s_waitcnt lgkmcnt(8)
	v_mfma_f32_32x32x16_f16 v[20:35], v[144:147], v[44:47], v[20:35]
	v_exp_f32_e32 v64, v64
	v_exp_f32_e32 v65, v65
	v_exp_f32_e32 v66, v66
	v_exp_f32_e32 v67, v67
	ds_read_b64_tr_b16 v[160:161], v211 offset:57344
	ds_read_b64_tr_b16 v[162:163], v211 offset:57856
	s_waitcnt lgkmcnt(9)
	v_mfma_f32_32x32x16_bf16 v[68:83], v[48:51], v[140:143], -4.0
	v_cvt_pk_f16_f32 v124, v84, v85
	v_pk_add_f16 v0, v0, v146
	v_pk_add_f16 v116, v164, v147
	v_cvt_pk_f16_f32 v125, v86, v87
	ds_read_b64_tr_b16 v[84:85], v211 offset:61440
	ds_read_b64_tr_b16 v[86:87], v211 offset:61952
	s_waitcnt lgkmcnt(10)
	v_mfma_f32_32x32x16_bf16 v[36:51], v[100:103], v[140:143], -4.0
	s_nop 0
	v_pk_add_f16 v0, v0, v124
	v_pk_add_f16 v100, v116, v125
	v_cvt_pk_f16_f32 v126, v88, v89
	v_cvt_pk_f16_f32 v127, v90, v91
	ds_read_b64_tr_b16 v[88:89], v211 offset:58368
	ds_read_b64_tr_b16 v[90:91], v211 offset:58880
	s_waitcnt lgkmcnt(11)
	v_mfma_f32_32x32x16_bf16 v[68:83], v[104:107], v[128:131], v[68:83]
	v_pk_add_f16 v0, v0, v126
	v_pk_add_f16 v100, v100, v127
	v_cvt_pk_f16_f32 v120, v92, v93
	v_cvt_pk_f16_f32 v121, v94, v95
	ds_read_b64_tr_b16 v[92:93], v211 offset:62464
	ds_read_b64_tr_b16 v[94:95], v211 offset:62976
	s_waitcnt lgkmcnt(12)
	v_mfma_f32_32x32x16_bf16 v[36:51], v[108:111], v[128:131], v[36:51]
	s_nop 0
	v_pk_add_f16 v0, v0, v120
	v_pk_add_f16 v100, v100, v121
	v_cvt_pk_f16_f32 v122, v96, v97
	v_cvt_pk_f16_f32 v123, v98, v99
	ds_read_b64_tr_b16 v[96:97], v211 offset:59392
	ds_read_b64_tr_b16 v[98:99], v211 offset:59904
	s_waitcnt lgkmcnt(13)
	v_mfma_f32_32x32x16_bf16 v[68:83], v[112:115], v[136:139], v[68:83]
	v_pk_add_f16 v0, v0, v122
	v_pk_add_f16 v100, v100, v123
	v_cvt_pk_f16_f32 v116, v52, v53
	v_cvt_pk_f16_f32 v117, v54, v55
	ds_read_b64_tr_b16 v[52:53], v211 offset:63488
	ds_read_b64_tr_b16 v[54:55], v211 offset:64000
	s_waitcnt lgkmcnt(14)
	v_mfma_f32_32x32x16_bf16 v[36:51], v[148:151], v[136:139], v[36:51]
	s_nop 0
	v_pk_add_f16 v0, v0, v116
	v_pk_add_f16 v100, v100, v117
	v_cvt_pk_f16_f32 v118, v56, v57
	v_cvt_pk_f16_f32 v119, v58, v59
	ds_read_b64_tr_b16 v[56:57], v211 offset:60416
	ds_read_b64_tr_b16 v[58:59], v211 offset:60928
	s_waitcnt lgkmcnt(14)
	v_mfma_f32_32x32x16_bf16 v[68:83], v[152:155], v[132:135], v[68:83]
	v_pk_add_f16 v0, v0, v118
	v_pk_add_f16 v100, v100, v119
	v_cvt_pk_f16_f32 v144, v60, v61
	v_cvt_pk_f16_f32 v145, v62, v63
	ds_read_b64_tr_b16 v[60:61], v211 offset:64512
	ds_read_b64_tr_b16 v[62:63], v211 offset:65024
	v_mfma_f32_32x32x16_bf16 v[36:51], v[156:159], v[132:135], v[36:51]
	s_nop 0
	v_pk_add_f16 v0, v0, v144
	v_pk_add_f16 v164, v100, v145
	v_cvt_pk_f16_f32 v146, v64, v65
	v_cvt_pk_f16_f32 v147, v66, v67
	s_waitcnt lgkmcnt(14)
	v_mfma_f32_32x32x16_f16 v[4:19], v[124:127], v[160:163], v[4:19]
	v_exp_f32_e32 v68, v68
	v_exp_f32_e32 v69, v69
	v_exp_f32_e32 v70, v70
	v_exp_f32_e32 v71, v71
	s_waitcnt lgkmcnt(12)
	v_mfma_f32_32x32x16_f16 v[20:35], v[124:127], v[84:87], v[20:35]
	v_exp_f32_e32 v72, v72
	v_exp_f32_e32 v73, v73
	v_exp_f32_e32 v74, v74
	v_exp_f32_e32 v75, v75
	ds_read_b128 v[84:87], v210 offset:24576
	ds_read_b128 v[104:107], v210 offset:26624
	s_waitcnt lgkmcnt(12)
	v_mfma_f32_32x32x16_f16 v[4:19], v[120:123], v[88:91], v[4:19]
	v_exp_f32_e32 v76, v76
	v_exp_f32_e32 v77, v77
	v_exp_f32_e32 v78, v78
	v_exp_f32_e32 v79, v79
	ds_read_b128 v[108:111], v210 offset:25088
	ds_read_b128 v[112:115], v210 offset:27136
	s_waitcnt lgkmcnt(12)
	v_mfma_f32_32x32x16_f16 v[20:35], v[120:123], v[92:95], v[20:35]
	v_exp_f32_e32 v80, v80
	v_exp_f32_e32 v81, v81
	v_exp_f32_e32 v82, v82
	v_exp_f32_e32 v83, v83
	ds_read_b128 v[148:151], v210 offset:28672
	ds_read_b128 v[152:155], v210 offset:30720
	s_waitcnt lgkmcnt(12)
	v_mfma_f32_32x32x16_f16 v[4:19], v[116:119], v[96:99], v[4:19]
	v_exp_f32_e32 v36, v36
	v_exp_f32_e32 v37, v37
	v_exp_f32_e32 v38, v38
	v_exp_f32_e32 v39, v39
	ds_read_b128 v[156:159], v210 offset:29184
	ds_read_b128 v[160:163], v210 offset:31232
	s_waitcnt lgkmcnt(12)
	v_mfma_f32_32x32x16_f16 v[20:35], v[116:119], v[52:55], v[20:35]
	v_exp_f32_e32 v40, v40
	v_exp_f32_e32 v41, v41
	v_exp_f32_e32 v42, v42
	v_exp_f32_e32 v43, v43
	s_waitcnt lgkmcnt(10)
	v_mfma_f32_32x32x16_f16 v[4:19], v[144:147], v[56:59], v[4:19]
	v_exp_f32_e32 v44, v44
	v_exp_f32_e32 v45, v45
	v_exp_f32_e32 v46, v46
	v_exp_f32_e32 v47, v47
	s_waitcnt lgkmcnt(8)
	v_mfma_f32_32x32x16_f16 v[20:35], v[144:147], v[60:63], v[20:35]
	v_exp_f32_e32 v48, v48
	v_exp_f32_e32 v49, v49
	v_exp_f32_e32 v50, v50
	v_exp_f32_e32 v51, v51
	s_waitcnt vmcnt(0) lgkmcnt(0)
	s_barrier
	ds_read_b64_tr_b16 v[100:101], v212 offset:16384
	ds_read_b64_tr_b16 v[102:103], v212 offset:16896
	s_waitcnt lgkmcnt(9)
	v_mfma_f32_32x32x16_bf16 v[52:67], v[84:87], v[140:143], -4.0
	v_mov_b32_e32 v116, v3
	v_pk_add_f16 v0, v0, v146
	v_pk_add_f16 v84, v164, v147
	v_cvt_pk_f16_f32 v124, v68, v69
	v_pk_add_f16 v0, v0, v84
	v_cvt_pk_f16_f32 v125, v70, v71
	v_dot2c_f32_f16_e32 v2, 0x3c003c00, v0
	v_mov_b32_e32 v0, v3
	ds_read_b64_tr_b16 v[68:69], v212 offset:20480
	ds_read_b64_tr_b16 v[70:71], v212 offset:20992
	s_waitcnt lgkmcnt(10)
	v_mfma_f32_32x32x16_bf16 v[84:99], v[104:107], v[140:143], -4.0
	s_nop 0
	v_pk_add_f16 v0, v0, v124
	v_pk_add_f16 v104, v116, v125
	v_cvt_pk_f16_f32 v126, v72, v73
	v_cvt_pk_f16_f32 v127, v74, v75
	ds_read_b64_tr_b16 v[72:73], v212 offset:17408
	ds_read_b64_tr_b16 v[74:75], v212 offset:17920
	s_waitcnt lgkmcnt(11)
	v_mfma_f32_32x32x16_bf16 v[52:67], v[108:111], v[128:131], v[52:67]
	v_pk_add_f16 v0, v0, v126
	v_pk_add_f16 v104, v104, v127
	v_cvt_pk_f16_f32 v120, v76, v77
	v_cvt_pk_f16_f32 v121, v78, v79
	ds_read_b64_tr_b16 v[76:77], v212 offset:21504
	ds_read_b64_tr_b16 v[78:79], v212 offset:22016
	s_waitcnt lgkmcnt(12)
	v_mfma_f32_32x32x16_bf16 v[84:99], v[112:115], v[128:131], v[84:99]
	v_pk_add_f16 v0, v0, v120
	v_pk_add_f16 v104, v104, v121
	v_cvt_pk_f16_f32 v122, v80, v81
	v_cvt_pk_f16_f32 v123, v82, v83
	ds_read_b64_tr_b16 v[80:81], v212 offset:18432
	ds_read_b64_tr_b16 v[82:83], v212 offset:18944
	s_waitcnt lgkmcnt(13)
	v_mfma_f32_32x32x16_bf16 v[52:67], v[148:151], v[136:139], v[52:67]
	v_pk_add_f16 v0, v0, v122
	v_pk_add_f16 v104, v104, v123
	v_cvt_pk_f16_f32 v116, v36, v37
	v_cvt_pk_f16_f32 v117, v38, v39
	ds_read_b64_tr_b16 v[36:37], v212 offset:22528
	ds_read_b64_tr_b16 v[38:39], v212 offset:23040
	s_waitcnt lgkmcnt(14)
	v_mfma_f32_32x32x16_bf16 v[84:99], v[152:155], v[136:139], v[84:99]
	v_pk_add_f16 v0, v0, v116
	v_pk_add_f16 v104, v104, v117
	v_cvt_pk_f16_f32 v118, v40, v41
	v_cvt_pk_f16_f32 v119, v42, v43
	ds_read_b64_tr_b16 v[40:41], v212 offset:19456
	ds_read_b64_tr_b16 v[42:43], v212 offset:19968
	s_waitcnt lgkmcnt(14)
	v_mfma_f32_32x32x16_bf16 v[52:67], v[156:159], v[132:135], v[52:67]
	v_pk_add_f16 v0, v0, v118
	v_pk_add_f16 v104, v104, v119
	v_cvt_pk_f16_f32 v144, v44, v45
	v_cvt_pk_f16_f32 v145, v46, v47
	ds_read_b64_tr_b16 v[44:45], v212 offset:23552
	ds_read_b64_tr_b16 v[46:47], v212 offset:24064
	v_mfma_f32_32x32x16_bf16 v[84:99], v[160:163], v[132:135], v[84:99]
	v_pk_add_f16 v0, v0, v144
	v_pk_add_f16 v104, v104, v145
	v_cvt_pk_f16_f32 v146, v48, v49
	v_cvt_pk_f16_f32 v147, v50, v51
	s_nop 0
	v_exp_f32_e32 v52, v52
	v_exp_f32_e32 v53, v53
	v_exp_f32_e32 v54, v54
	v_exp_f32_e32 v55, v55
	s_nop 0
	v_exp_f32_e32 v56, v56
	v_exp_f32_e32 v57, v57
	v_exp_f32_e32 v58, v58
	v_exp_f32_e32 v59, v59
	s_nop 0
	v_exp_f32_e32 v60, v60
	v_exp_f32_e32 v61, v61
	v_exp_f32_e32 v62, v62
	v_exp_f32_e32 v63, v63
	s_nop 0
	v_exp_f32_e32 v64, v64
	v_exp_f32_e32 v65, v65
	v_exp_f32_e32 v66, v66
	v_exp_f32_e32 v67, v67
	v_exp_f32_e32 v84, v84
	v_exp_f32_e32 v85, v85
	v_exp_f32_e32 v86, v86
	v_exp_f32_e32 v87, v87
	s_nop 0
	v_exp_f32_e32 v88, v88
	v_exp_f32_e32 v89, v89
	v_exp_f32_e32 v90, v90
	v_exp_f32_e32 v91, v91
	s_nop 0
	v_exp_f32_e32 v92, v92
	v_exp_f32_e32 v93, v93
	v_exp_f32_e32 v94, v94
	v_exp_f32_e32 v95, v95
	s_nop 0
	v_exp_f32_e32 v96, v96
	v_exp_f32_e32 v97, v97
	v_exp_f32_e32 v98, v98
	v_exp_f32_e32 v99, v99
	s_waitcnt lgkmcnt(14)
	v_mfma_f32_32x32x16_f16 v[4:19], v[124:127], v[100:103], v[4:19]
	v_pk_add_f16 v0, v0, v146
	v_cvt_pk_f16_f32 v48, v52, v53
	v_cvt_pk_f16_f32 v52, v60, v61
	v_cvt_pk_f16_f32 v49, v54, v55
	v_cvt_pk_f16_f32 v50, v56, v57
	v_cvt_pk_f16_f32 v54, v64, v65
	v_cvt_pk_f16_f32 v56, v84, v85
	s_waitcnt lgkmcnt(12)
	v_mfma_f32_32x32x16_f16 v[20:35], v[124:127], v[68:71], v[20:35]
	v_pk_add_f16 v68, v104, v147
	v_cvt_pk_f16_f32 v60, v92, v93
	v_pk_add_f16 v0, v0, v48
	v_pk_add_f16 v64, v68, v52
	v_cvt_pk_f16_f32 v53, v62, v63
	v_pk_add_f16 v0, v0, v56
	v_pk_add_f16 v64, v64, v60
	s_waitcnt lgkmcnt(10)
	v_mfma_f32_32x32x16_f16 v[4:19], v[120:123], v[72:75], v[4:19]
	v_cvt_pk_f16_f32 v57, v86, v87
	v_cvt_pk_f16_f32 v61, v94, v95
	v_pk_add_f16 v0, v0, v49
	v_cvt_pk_f16_f32 v51, v58, v59
	v_pk_add_f16 v0, v0, v57
	v_cvt_pk_f16_f32 v58, v88, v89
	v_cvt_pk_f16_f32 v62, v96, v97
	s_waitcnt lgkmcnt(8)
	v_mfma_f32_32x32x16_f16 v[20:35], v[120:123], v[76:79], v[20:35]
	v_pk_add_f16 v0, v0, v50
	v_cvt_pk_f16_f32 v55, v66, v67
	v_pk_add_f16 v0, v0, v58
	v_cvt_pk_f16_f32 v59, v90, v91
	v_cvt_pk_f16_f32 v63, v98, v99
	v_pk_add_f16 v0, v0, v51
	s_waitcnt lgkmcnt(6)
	v_mfma_f32_32x32x16_f16 v[4:19], v[116:119], v[80:83], v[4:19]
	v_pk_add_f16 v0, v0, v59
	s_waitcnt lgkmcnt(4)
	v_mfma_f32_32x32x16_f16 v[20:35], v[116:119], v[36:39], v[20:35]
	v_pk_add_f16 v36, v64, v53
	s_nop 0
	v_pk_add_f16 v36, v36, v61
	s_nop 0
	v_pk_add_f16 v36, v36, v54
	s_nop 0
	v_pk_add_f16 v36, v36, v62
	s_waitcnt lgkmcnt(2)
	v_mfma_f32_32x32x16_f16 v[4:19], v[144:147], v[40:43], v[4:19]
	v_pk_add_f16 v36, v36, v55
	s_nop 0
	v_pk_add_f16 v36, v36, v63
	s_nop 0
	v_pk_add_f16 v0, v36, v0
	s_nop 0
	v_dot2c_f32_f16_e32 v2, 0x3c003c00, v0
	s_waitcnt lgkmcnt(0)
	v_mfma_f32_32x32x16_f16 v[20:35], v[144:147], v[44:47], v[20:35]
	ds_read_b64_tr_b16 v[36:37],v214 offset:0
	ds_read_b64_tr_b16 v[38:39],v214 offset:512
	ds_read_b64_tr_b16 v[40:41],v214 offset:1024
	ds_read_b64_tr_b16 v[42:43],v214 offset:1536
	ds_read_b64_tr_b16 v[44:45],v214 offset:2048
	ds_read_b64_tr_b16 v[46:47],v214 offset:2560
	ds_read_b64_tr_b16 v[64:65],v214 offset:3072
	ds_read_b64_tr_b16 v[66:67],v214 offset:3584
	s_waitcnt lgkmcnt(0)
	s_nop 0
	v_mfma_f32_32x32x16_f16 v[4:19], v[48:51], v[36:39], v[4:19]
	ds_read_b64_tr_b16 v[36:37],v214 offset:4096
	ds_read_b64_tr_b16 v[38:39],v214 offset:4608
	v_mfma_f32_32x32x16_f16 v[4:19], v[52:55], v[40:43], v[4:19]
	ds_read_b64_tr_b16 v[40:41],v214 offset:5120
	ds_read_b64_tr_b16 v[42:43],v214 offset:5632
	v_mfma_f32_32x32x16_f16 v[4:19], v[56:59], v[44:47], v[4:19]
	ds_read_b64_tr_b16 v[44:45],v214 offset:6144
	ds_read_b64_tr_b16 v[46:47],v214 offset:6656
	v_mfma_f32_32x32x16_f16 v[4:19], v[60:63], v[64:67], v[4:19]
	ds_read_b64_tr_b16 v[64:65],v214 offset:7168
	ds_read_b64_tr_b16 v[66:67],v214 offset:7680
	s_waitcnt lgkmcnt(0)
	v_mfma_f32_32x32x16_f16 v[20:35], v[48:51], v[36:39], v[20:35]
	v_mov_b32_e32 v36, v2
	s_nop 1
	v_permlane32_swap_b32_e32 v2, v36
	v_mfma_f32_32x32x16_f16 v[20:35], v[52:55], v[40:43], v[20:35]
	v_mfma_f32_32x32x16_f16 v[20:35], v[56:59], v[44:47], v[20:35]
	v_mfma_f32_32x32x16_f16 v[20:35], v[60:63], v[64:67], v[20:35]
	s_and_saveexec_b64 s[14:15], s[4:5]
	s_cbranch_execz .LBB0_241
	v_add_f32_e32 v0, v2, v36
	v_lshl_add_u32 v2, v207, 2, s11
	ds_write_b32 v2, v0 offset:128
	s_branch .LBB0_241
